# baseline (speedup 1.0000x reference)
.LBB5_4:
	s_load_dwordx2 s[2:3], s[0:1], 0x14
	v_lshrrev_b32_e32 v3, 4, v0
	s_lshl_b32 s12, s15, 7
	s_lshl_b32 s13, s14, 7
	v_xor_b32_e32 v1, v3, v0
	s_waitcnt lgkmcnt(0)
	s_ashr_i32 s14, s3, 31
	s_mul_i32 s0, s12, s14
	s_mul_hi_u32 s1, s12, s3
	v_lshlrev_b32_e32 v1, 3, v1
	v_or_b32_e32 v4, 0x200, v0
	s_add_i32 s1, s1, s0
	s_mul_i32 s0, s12, s3
	v_and_b32_e32 v2, 56, v1
	v_lshrrev_b32_e32 v1, 3, v0
	v_lshrrev_b32_e32 v4, 3, v4
	s_lshl_b64 s[0:1], s[0:1], 1
	v_mul_lo_u32 v1, v1, s3
	v_mul_lo_u32 v4, v4, s3
	s_add_u32 s0, s4, s0
	v_add_lshl_u32 v1, v1, v2, 1
	v_add_lshl_u32 v2, v4, v2, 1
	s_addc_u32 s1, s5, s1
	s_mul_i32 s4, s13, s14
	s_mul_hi_u32 s5, s13, s3
	v_lshl_add_u32 v4, v0, 4, 0
	s_add_i32 s5, s5, s4
	s_mul_i32 s4, s13, s3
	v_readfirstlane_b32 s18, v4
	v_add_u32_e32 v5, 0x2000, v4
	s_lshl_b64 s[4:5], s[4:5], 1
	s_mov_b32 m0, s18
	v_readfirstlane_b32 s15, v5
	v_add_u32_e32 v5, 0x4000, v4
	s_add_u32 s4, s6, s4
	global_load_lds_dwordx4 v1, s[0:1]
	s_mov_b32 m0, s15
	v_readfirstlane_b32 s16, v5
	v_add_u32_e32 v5, 0x6000, v4
	s_addc_u32 s5, s7, s5
	global_load_lds_dwordx4 v2, s[0:1]
	s_mov_b32 m0, s16
	v_readfirstlane_b32 s17, v5
	v_add_u32_e32 v5, 0x8000, v4
	global_load_lds_dwordx4 v1, s[4:5]
	s_mov_b32 m0, s17
	s_add_u32 s6, s0, 0x80
	v_readfirstlane_b32 s14, v5
	v_add_u32_e32 v5, 0xa000, v4
	global_load_lds_dwordx4 v2, s[4:5]
	s_addc_u32 s7, s1, 0
	s_mov_b32 m0, s14
	v_readfirstlane_b32 s3, v5
	global_load_lds_dwordx4 v1, s[6:7]
	s_mov_b32 m0, s3
	v_add_u32_e32 v5, 0xc000, v4
	s_add_u32 s20, s4, 0x80
	global_load_lds_dwordx4 v2, s[6:7]
	v_readfirstlane_b32 s6, v5
	v_add_u32_e32 v4, 0xe000, v4
	s_addc_u32 s21, s5, 0
	s_mov_b32 m0, s6
	v_readfirstlane_b32 s7, v4
	global_load_lds_dwordx4 v1, s[20:21]
	s_mov_b32 m0, s7
	v_lshrrev_b32_e32 v5, 1, v0
	global_load_lds_dwordx4 v2, s[20:21]
	v_bfe_u32 v6, v0, 1, 3
	v_and_b32_e32 v4, 15, v0
	v_lshrrev_b32_e32 v7, 2, v0
	v_bitop3_b32 v3, v3, v6, 3 bitop3:0x6c
	v_and_b32_e32 v8, 0x60, v5
	v_and_or_b32 v32, v7, 64, v4
	v_lshlrev_b32_e32 v7, 4, v3
	v_or_b32_e32 v3, v8, v4
	v_lshl_add_u32 v4, v3, 7, 0
	s_waitcnt vmcnt(4)
	s_barrier
	v_add_u32_e32 v3, v4, v7
	ds_read_b128 v[10:13], v3 offset:16384
	v_lshl_add_u32 v30, v32, 7, 0
	v_add_u32_e32 v5, v30, v7
	ds_read_b128 v[14:17], v5
	ds_read_b128 v[18:21], v3 offset:18432
	ds_read_b128 v[22:25], v5 offset:2048
	ds_read_b128 v[34:37], v5 offset:4096
	ds_read_b128 v[38:41], v5 offset:6144
	v_bfe_u32 v9, v0, 4, 2
	v_bitop3_b32 v0, v9, v6, 4 bitop3:0x36
	s_waitcnt lgkmcnt(0)
	v_mfma_f32_16x16x32_f16 v[26:29], v[10:13], v[14:17], 0
	v_lshlrev_b32_e32 v6, 4, v0
	v_mfma_f32_16x16x32_f16 v[14:17], v[18:21], v[14:17], 0
	v_add_u32_e32 v0, v30, v6
	ds_read_b128 v[42:45], v0
	ds_read_b128 v[46:49], v0 offset:2048
	ds_read_b128 v[50:53], v0 offset:4096
	ds_read_b128 v[54:57], v0 offset:6144
	v_add_u32_e32 v4, v4, v6
	ds_read_b128 v[58:61], v4 offset:16384
	ds_read_b128 v[62:65], v4 offset:18432
	v_mfma_f32_16x16x32_f16 v[66:69], v[10:13], v[22:25], 0
	v_mfma_f32_16x16x32_f16 v[22:25], v[18:21], v[22:25], 0
	v_mfma_f32_16x16x32_f16 v[70:73], v[10:13], v[34:37], 0
	v_mfma_f32_16x16x32_f16 v[34:37], v[18:21], v[34:37], 0
	v_mfma_f32_16x16x32_f16 v[10:13], v[10:13], v[38:41], 0
	v_mfma_f32_16x16x32_f16 v[18:21], v[18:21], v[38:41], 0
	s_add_u32 s20, s0, 0x100
	s_mov_b32 m0, s18
	s_waitcnt vmcnt(0) lgkmcnt(0)
	s_barrier
	s_addc_u32 s21, s1, 0
	s_add_u32 s22, s4, 0x100
	global_load_lds_dwordx4 v1, s[20:21]
	s_mov_b32 m0, s15
	s_addc_u32 s23, s5, 0
	global_load_lds_dwordx4 v2, s[20:21]
	s_mov_b32 m0, s16
	s_nop 0
	global_load_lds_dwordx4 v1, s[22:23]
	s_mov_b32 m0, s17
	s_nop 0
	global_load_lds_dwordx4 v2, s[22:23]
	s_waitcnt lgkmcnt(0)
	v_mfma_f32_16x16x32_f16 v[26:29], v[58:61], v[42:45], v[26:29]
	v_mfma_f32_16x16x32_f16 v[14:17], v[62:65], v[42:45], v[14:17]
	ds_read_b128 v[38:41], v5 offset:32768
	ds_read_b128 v[42:45], v5 offset:34816
	ds_read_b128 v[74:77], v5 offset:36864
	ds_read_b128 v[78:81], v5 offset:38912
	ds_read_b128 v[82:85], v3 offset:49152
	ds_read_b128 v[86:89], v3 offset:51200
	v_mfma_f32_16x16x32_f16 v[66:69], v[58:61], v[46:49], v[66:69]
	v_mfma_f32_16x16x32_f16 v[22:25], v[62:65], v[46:49], v[22:25]
	v_mfma_f32_16x16x32_f16 v[46:49], v[58:61], v[50:53], v[70:73]
	v_mfma_f32_16x16x32_f16 v[34:37], v[62:65], v[50:53], v[34:37]
	v_mfma_f32_16x16x32_f16 v[10:13], v[58:61], v[54:57], v[10:13]
	v_mfma_f32_16x16x32_f16 v[18:21], v[62:65], v[54:57], v[18:21]
	s_waitcnt lgkmcnt(0)
	v_mfma_f32_16x16x32_f16 v[26:29], v[82:85], v[38:41], v[26:29]
	v_mfma_f32_16x16x32_f16 v[14:17], v[86:89], v[38:41], v[14:17]
	ds_read_b128 v[38:41], v0 offset:32768
	ds_read_b128 v[50:53], v0 offset:34816
	ds_read_b128 v[54:57], v0 offset:36864
	ds_read_b128 v[58:61], v0 offset:38912
	ds_read_b128 v[62:65], v4 offset:49152
	ds_read_b128 v[70:73], v4 offset:51200
	v_mfma_f32_16x16x32_f16 v[66:69], v[82:85], v[42:45], v[66:69]
	v_mfma_f32_16x16x32_f16 v[22:25], v[86:89], v[42:45], v[22:25]
	v_mfma_f32_16x16x32_f16 v[42:45], v[82:85], v[74:77], v[46:49]
	v_mfma_f32_16x16x32_f16 v[34:37], v[86:89], v[74:77], v[34:37]
	v_mfma_f32_16x16x32_f16 v[10:13], v[82:85], v[78:81], v[10:13]
	v_mfma_f32_16x16x32_f16 v[18:21], v[86:89], v[78:81], v[18:21]
	s_add_u32 s20, s0, 0x180
	s_mov_b32 m0, s14
	s_waitcnt vmcnt(0) lgkmcnt(0)
	s_barrier
	s_addc_u32 s21, s1, 0
	s_add_u32 s22, s4, 0x180
	global_load_lds_dwordx4 v1, s[20:21]
	s_mov_b32 m0, s3
	s_addc_u32 s23, s5, 0
	global_load_lds_dwordx4 v2, s[20:21]
	s_mov_b32 m0, s6
	s_nop 0
	global_load_lds_dwordx4 v1, s[22:23]
	s_mov_b32 m0, s7
	s_nop 0
	global_load_lds_dwordx4 v2, s[22:23]
	s_waitcnt lgkmcnt(0)
	v_mfma_f32_16x16x32_f16 v[26:29], v[62:65], v[38:41], v[26:29]
	v_mfma_f32_16x16x32_f16 v[14:17], v[70:73], v[38:41], v[14:17]
	ds_read_b128 v[38:41], v5
	ds_read_b128 v[46:49], v5 offset:2048
	ds_read_b128 v[74:77], v5 offset:4096
	ds_read_b128 v[78:81], v5 offset:6144
	ds_read_b128 v[82:85], v3 offset:16384
	ds_read_b128 v[86:89], v3 offset:18432
	v_mfma_f32_16x16x32_f16 v[66:69], v[62:65], v[50:53], v[66:69]
	v_mfma_f32_16x16x32_f16 v[22:25], v[70:73], v[50:53], v[22:25]
	v_mfma_f32_16x16x32_f16 v[42:45], v[62:65], v[54:57], v[42:45]
	v_mfma_f32_16x16x32_f16 v[34:37], v[70:73], v[54:57], v[34:37]
	v_mfma_f32_16x16x32_f16 v[10:13], v[62:65], v[58:61], v[10:13]
	v_mfma_f32_16x16x32_f16 v[18:21], v[70:73], v[58:61], v[18:21]
	s_waitcnt lgkmcnt(0)
	v_mfma_f32_16x16x32_f16 v[26:29], v[82:85], v[38:41], v[26:29]
	v_mfma_f32_16x16x32_f16 v[14:17], v[86:89], v[38:41], v[14:17]
	ds_read_b128 v[38:41], v0
	ds_read_b128 v[50:53], v0 offset:2048
	ds_read_b128 v[54:57], v0 offset:4096
	ds_read_b128 v[58:61], v0 offset:6144
	ds_read_b128 v[62:65], v4 offset:16384
	ds_read_b128 v[70:73], v4 offset:18432
	v_mfma_f32_16x16x32_f16 v[66:69], v[82:85], v[46:49], v[66:69]
	v_mfma_f32_16x16x32_f16 v[22:25], v[86:89], v[46:49], v[22:25]
	v_mfma_f32_16x16x32_f16 v[42:45], v[82:85], v[74:77], v[42:45]
	v_mfma_f32_16x16x32_f16 v[34:37], v[86:89], v[74:77], v[34:37]
	v_mfma_f32_16x16x32_f16 v[10:13], v[82:85], v[78:81], v[10:13]
	v_mfma_f32_16x16x32_f16 v[18:21], v[86:89], v[78:81], v[18:21]
	s_add_u32 s20, s0, 0x200
	s_mov_b32 m0, s18
	s_waitcnt vmcnt(0) lgkmcnt(0)
	s_barrier
	s_addc_u32 s21, s1, 0
	s_add_u32 s22, s4, 0x200
	global_load_lds_dwordx4 v1, s[20:21]
	s_mov_b32 m0, s15
	s_addc_u32 s23, s5, 0
	global_load_lds_dwordx4 v2, s[20:21]
	s_mov_b32 m0, s16
	s_nop 0
	global_load_lds_dwordx4 v1, s[22:23]
	s_mov_b32 m0, s17
	s_nop 0
	global_load_lds_dwordx4 v2, s[22:23]
	s_waitcnt lgkmcnt(0)
	v_mfma_f32_16x16x32_f16 v[26:29], v[62:65], v[38:41], v[26:29]
	v_mfma_f32_16x16x32_f16 v[14:17], v[70:73], v[38:41], v[14:17]
	ds_read_b128 v[38:41], v5 offset:32768
	ds_read_b128 v[46:49], v5 offset:34816
	ds_read_b128 v[74:77], v5 offset:36864
	ds_read_b128 v[78:81], v5 offset:38912
	ds_read_b128 v[82:85], v3 offset:49152
	ds_read_b128 v[86:89], v3 offset:51200
	v_mfma_f32_16x16x32_f16 v[66:69], v[62:65], v[50:53], v[66:69]
	v_mfma_f32_16x16x32_f16 v[22:25], v[70:73], v[50:53], v[22:25]
	v_mfma_f32_16x16x32_f16 v[42:45], v[62:65], v[54:57], v[42:45]
	v_mfma_f32_16x16x32_f16 v[34:37], v[70:73], v[54:57], v[34:37]
	v_mfma_f32_16x16x32_f16 v[10:13], v[62:65], v[58:61], v[10:13]
	v_mfma_f32_16x16x32_f16 v[18:21], v[70:73], v[58:61], v[18:21]
	s_waitcnt lgkmcnt(0)
	v_mfma_f32_16x16x32_f16 v[26:29], v[82:85], v[38:41], v[26:29]
	v_mfma_f32_16x16x32_f16 v[14:17], v[86:89], v[38:41], v[14:17]
	ds_read_b128 v[38:41], v0 offset:32768
	ds_read_b128 v[50:53], v0 offset:34816
	ds_read_b128 v[54:57], v0 offset:36864
	ds_read_b128 v[58:61], v0 offset:38912
	ds_read_b128 v[62:65], v4 offset:49152
	ds_read_b128 v[70:73], v4 offset:51200
	v_mfma_f32_16x16x32_f16 v[66:69], v[82:85], v[46:49], v[66:69]
	v_mfma_f32_16x16x32_f16 v[22:25], v[86:89], v[46:49], v[22:25]
	v_mfma_f32_16x16x32_f16 v[42:45], v[82:85], v[74:77], v[42:45]
	v_mfma_f32_16x16x32_f16 v[34:37], v[86:89], v[74:77], v[34:37]
	v_mfma_f32_16x16x32_f16 v[10:13], v[82:85], v[78:81], v[10:13]
	v_mfma_f32_16x16x32_f16 v[18:21], v[86:89], v[78:81], v[18:21]
	s_add_u32 s20, s0, 0x280
	s_mov_b32 m0, s14
	s_waitcnt vmcnt(0) lgkmcnt(0)
	s_barrier
	s_addc_u32 s21, s1, 0
	s_add_u32 s22, s4, 0x280
	global_load_lds_dwordx4 v1, s[20:21]
	s_mov_b32 m0, s3
	s_addc_u32 s23, s5, 0
	global_load_lds_dwordx4 v2, s[20:21]
	s_mov_b32 m0, s6
	s_nop 0
	global_load_lds_dwordx4 v1, s[22:23]
	s_mov_b32 m0, s7
	s_nop 0
	global_load_lds_dwordx4 v2, s[22:23]
	s_waitcnt lgkmcnt(0)
	v_mfma_f32_16x16x32_f16 v[26:29], v[62:65], v[38:41], v[26:29]
	v_mfma_f32_16x16x32_f16 v[14:17], v[70:73], v[38:41], v[14:17]
	ds_read_b128 v[38:41], v5
	ds_read_b128 v[46:49], v5 offset:2048
	ds_read_b128 v[74:77], v5 offset:4096
	ds_read_b128 v[78:81], v5 offset:6144
	ds_read_b128 v[82:85], v3 offset:16384
	ds_read_b128 v[86:89], v3 offset:18432
	v_mfma_f32_16x16x32_f16 v[66:69], v[62:65], v[50:53], v[66:69]
	v_mfma_f32_16x16x32_f16 v[22:25], v[70:73], v[50:53], v[22:25]
	v_mfma_f32_16x16x32_f16 v[42:45], v[62:65], v[54:57], v[42:45]
	v_mfma_f32_16x16x32_f16 v[34:37], v[70:73], v[54:57], v[34:37]
	v_mfma_f32_16x16x32_f16 v[10:13], v[62:65], v[58:61], v[10:13]
	v_mfma_f32_16x16x32_f16 v[18:21], v[70:73], v[58:61], v[18:21]
	s_waitcnt lgkmcnt(0)
	v_mfma_f32_16x16x32_f16 v[26:29], v[82:85], v[38:41], v[26:29]
	v_mfma_f32_16x16x32_f16 v[14:17], v[86:89], v[38:41], v[14:17]
	ds_read_b128 v[38:41], v0
	ds_read_b128 v[50:53], v0 offset:2048
	ds_read_b128 v[54:57], v0 offset:4096
	ds_read_b128 v[58:61], v0 offset:6144
	ds_read_b128 v[62:65], v4 offset:16384
	ds_read_b128 v[70:73], v4 offset:18432
	v_mfma_f32_16x16x32_f16 v[66:69], v[82:85], v[46:49], v[66:69]
	v_mfma_f32_16x16x32_f16 v[22:25], v[86:89], v[46:49], v[22:25]
	v_mfma_f32_16x16x32_f16 v[42:45], v[82:85], v[74:77], v[42:45]
	v_mfma_f32_16x16x32_f16 v[34:37], v[86:89], v[74:77], v[34:37]
	v_mfma_f32_16x16x32_f16 v[10:13], v[82:85], v[78:81], v[10:13]
	v_mfma_f32_16x16x32_f16 v[18:21], v[86:89], v[78:81], v[18:21]
	s_add_u32 s20, s0, 0x300
	s_mov_b32 m0, s18
	s_waitcnt vmcnt(0) lgkmcnt(0)
	s_barrier
	s_addc_u32 s21, s1, 0
	s_add_u32 s22, s4, 0x300
	global_load_lds_dwordx4 v1, s[20:21]
	s_mov_b32 m0, s15
	s_addc_u32 s23, s5, 0
	global_load_lds_dwordx4 v2, s[20:21]
	s_mov_b32 m0, s16
	s_nop 0
	global_load_lds_dwordx4 v1, s[22:23]
	s_mov_b32 m0, s17
	s_nop 0
	global_load_lds_dwordx4 v2, s[22:23]
	s_waitcnt lgkmcnt(0)
	v_mfma_f32_16x16x32_f16 v[26:29], v[62:65], v[38:41], v[26:29]
	v_mfma_f32_16x16x32_f16 v[14:17], v[70:73], v[38:41], v[14:17]
	ds_read_b128 v[38:41], v5 offset:32768
	ds_read_b128 v[46:49], v5 offset:34816
	ds_read_b128 v[74:77], v5 offset:36864
	ds_read_b128 v[78:81], v5 offset:38912
	ds_read_b128 v[82:85], v3 offset:49152
	ds_read_b128 v[86:89], v3 offset:51200
	v_mfma_f32_16x16x32_f16 v[66:69], v[62:65], v[50:53], v[66:69]
	v_mfma_f32_16x16x32_f16 v[22:25], v[70:73], v[50:53], v[22:25]
	v_mfma_f32_16x16x32_f16 v[42:45], v[62:65], v[54:57], v[42:45]
	v_mfma_f32_16x16x32_f16 v[34:37], v[70:73], v[54:57], v[34:37]
	v_mfma_f32_16x16x32_f16 v[10:13], v[62:65], v[58:61], v[10:13]
	v_mfma_f32_16x16x32_f16 v[18:21], v[70:73], v[58:61], v[18:21]
	s_waitcnt lgkmcnt(0)
	v_mfma_f32_16x16x32_f16 v[26:29], v[82:85], v[38:41], v[26:29]
	v_mfma_f32_16x16x32_f16 v[14:17], v[86:89], v[38:41], v[14:17]
	ds_read_b128 v[38:41], v0 offset:32768
	ds_read_b128 v[50:53], v0 offset:34816
	ds_read_b128 v[54:57], v0 offset:36864
	ds_read_b128 v[58:61], v0 offset:38912
	ds_read_b128 v[62:65], v4 offset:49152
	ds_read_b128 v[70:73], v4 offset:51200
	v_mfma_f32_16x16x32_f16 v[66:69], v[82:85], v[46:49], v[66:69]
	v_mfma_f32_16x16x32_f16 v[22:25], v[86:89], v[46:49], v[22:25]
	v_mfma_f32_16x16x32_f16 v[42:45], v[82:85], v[74:77], v[42:45]
	v_mfma_f32_16x16x32_f16 v[34:37], v[86:89], v[74:77], v[34:37]
	v_mfma_f32_16x16x32_f16 v[10:13], v[82:85], v[78:81], v[10:13]
	v_mfma_f32_16x16x32_f16 v[18:21], v[86:89], v[78:81], v[18:21]
	s_add_u32 s20, s0, 0x380
	s_mov_b32 m0, s14
	s_waitcnt vmcnt(0) lgkmcnt(0)
	s_barrier
	s_addc_u32 s21, s1, 0
	s_add_u32 s22, s4, 0x380
	global_load_lds_dwordx4 v1, s[20:21]
	s_mov_b32 m0, s3
	s_addc_u32 s23, s5, 0
	global_load_lds_dwordx4 v2, s[20:21]
	s_mov_b32 m0, s6
	s_nop 0
	global_load_lds_dwordx4 v1, s[22:23]
	s_mov_b32 m0, s7
	s_nop 0
	global_load_lds_dwordx4 v2, s[22:23]
	s_waitcnt lgkmcnt(0)
	v_mfma_f32_16x16x32_f16 v[26:29], v[62:65], v[38:41], v[26:29]
	v_mfma_f32_16x16x32_f16 v[14:17], v[70:73], v[38:41], v[14:17]
	ds_read_b128 v[38:41], v5
	ds_read_b128 v[46:49], v5 offset:2048
	ds_read_b128 v[74:77], v5 offset:4096
	ds_read_b128 v[78:81], v5 offset:6144
	ds_read_b128 v[82:85], v3 offset:16384
	ds_read_b128 v[86:89], v3 offset:18432
	v_mfma_f32_16x16x32_f16 v[66:69], v[62:65], v[50:53], v[66:69]
	v_mfma_f32_16x16x32_f16 v[22:25], v[70:73], v[50:53], v[22:25]
	v_mfma_f32_16x16x32_f16 v[42:45], v[62:65], v[54:57], v[42:45]
	v_mfma_f32_16x16x32_f16 v[34:37], v[70:73], v[54:57], v[34:37]
	v_mfma_f32_16x16x32_f16 v[10:13], v[62:65], v[58:61], v[10:13]
	v_mfma_f32_16x16x32_f16 v[18:21], v[70:73], v[58:61], v[18:21]
	s_waitcnt lgkmcnt(0)
	v_mfma_f32_16x16x32_f16 v[26:29], v[82:85], v[38:41], v[26:29]
	v_mfma_f32_16x16x32_f16 v[14:17], v[86:89], v[38:41], v[14:17]
	ds_read_b128 v[38:41], v0
	ds_read_b128 v[50:53], v0 offset:2048
	ds_read_b128 v[54:57], v0 offset:4096
	ds_read_b128 v[58:61], v0 offset:6144
	ds_read_b128 v[62:65], v4 offset:16384
	ds_read_b128 v[70:73], v4 offset:18432
	v_mfma_f32_16x16x32_f16 v[66:69], v[82:85], v[46:49], v[66:69]
	v_mfma_f32_16x16x32_f16 v[22:25], v[86:89], v[46:49], v[22:25]
	v_mfma_f32_16x16x32_f16 v[42:45], v[82:85], v[74:77], v[42:45]
	v_mfma_f32_16x16x32_f16 v[34:37], v[86:89], v[74:77], v[34:37]
	v_mfma_f32_16x16x32_f16 v[10:13], v[82:85], v[78:81], v[10:13]
	v_mfma_f32_16x16x32_f16 v[18:21], v[86:89], v[78:81], v[18:21]
	s_add_u32 s20, s0, 0x400
	s_mov_b32 m0, s18
	s_waitcnt vmcnt(0) lgkmcnt(0)
	s_barrier
	s_addc_u32 s21, s1, 0
	s_add_u32 s22, s4, 0x400
	global_load_lds_dwordx4 v1, s[20:21]
	s_mov_b32 m0, s15
	s_addc_u32 s23, s5, 0
	global_load_lds_dwordx4 v2, s[20:21]
	s_mov_b32 m0, s16
	s_nop 0
	global_load_lds_dwordx4 v1, s[22:23]
	s_mov_b32 m0, s17
	s_nop 0
	global_load_lds_dwordx4 v2, s[22:23]
	s_waitcnt lgkmcnt(0)
	v_mfma_f32_16x16x32_f16 v[26:29], v[62:65], v[38:41], v[26:29]
	v_mfma_f32_16x16x32_f16 v[14:17], v[70:73], v[38:41], v[14:17]
	ds_read_b128 v[38:41], v5 offset:32768
	ds_read_b128 v[46:49], v5 offset:34816
	ds_read_b128 v[74:77], v5 offset:36864
	ds_read_b128 v[78:81], v5 offset:38912
	ds_read_b128 v[82:85], v3 offset:49152
	ds_read_b128 v[86:89], v3 offset:51200
	v_mfma_f32_16x16x32_f16 v[66:69], v[62:65], v[50:53], v[66:69]
	v_mfma_f32_16x16x32_f16 v[22:25], v[70:73], v[50:53], v[22:25]
	v_mfma_f32_16x16x32_f16 v[42:45], v[62:65], v[54:57], v[42:45]
	v_mfma_f32_16x16x32_f16 v[34:37], v[70:73], v[54:57], v[34:37]
	v_mfma_f32_16x16x32_f16 v[10:13], v[62:65], v[58:61], v[10:13]
	v_mfma_f32_16x16x32_f16 v[18:21], v[70:73], v[58:61], v[18:21]
	s_waitcnt lgkmcnt(0)
	v_mfma_f32_16x16x32_f16 v[26:29], v[82:85], v[38:41], v[26:29]
	v_mfma_f32_16x16x32_f16 v[14:17], v[86:89], v[38:41], v[14:17]
	ds_read_b128 v[38:41], v0 offset:32768
	ds_read_b128 v[50:53], v0 offset:34816
	ds_read_b128 v[54:57], v0 offset:36864
	ds_read_b128 v[58:61], v0 offset:38912
	ds_read_b128 v[62:65], v4 offset:49152
	ds_read_b128 v[70:73], v4 offset:51200
	v_mfma_f32_16x16x32_f16 v[66:69], v[82:85], v[46:49], v[66:69]
	v_mfma_f32_16x16x32_f16 v[22:25], v[86:89], v[46:49], v[22:25]
	v_mfma_f32_16x16x32_f16 v[42:45], v[82:85], v[74:77], v[42:45]
	v_mfma_f32_16x16x32_f16 v[34:37], v[86:89], v[74:77], v[34:37]
	v_mfma_f32_16x16x32_f16 v[10:13], v[82:85], v[78:81], v[10:13]
	v_mfma_f32_16x16x32_f16 v[18:21], v[86:89], v[78:81], v[18:21]
	s_add_u32 s20, s0, 0x480
	s_mov_b32 m0, s14
	s_waitcnt vmcnt(0) lgkmcnt(0)
	s_barrier
	s_addc_u32 s21, s1, 0
	s_add_u32 s22, s4, 0x480
	global_load_lds_dwordx4 v1, s[20:21]
	s_mov_b32 m0, s3
	s_addc_u32 s23, s5, 0
	global_load_lds_dwordx4 v2, s[20:21]
	s_mov_b32 m0, s6
	s_nop 0
	global_load_lds_dwordx4 v1, s[22:23]
	s_mov_b32 m0, s7
	s_nop 0
	global_load_lds_dwordx4 v2, s[22:23]
	s_waitcnt lgkmcnt(0)
	v_mfma_f32_16x16x32_f16 v[26:29], v[62:65], v[38:41], v[26:29]
	v_mfma_f32_16x16x32_f16 v[14:17], v[70:73], v[38:41], v[14:17]
	ds_read_b128 v[38:41], v5
	ds_read_b128 v[46:49], v5 offset:2048
	ds_read_b128 v[74:77], v5 offset:4096
	ds_read_b128 v[78:81], v5 offset:6144
	ds_read_b128 v[82:85], v3 offset:16384
	ds_read_b128 v[86:89], v3 offset:18432
	v_mfma_f32_16x16x32_f16 v[66:69], v[62:65], v[50:53], v[66:69]
	v_mfma_f32_16x16x32_f16 v[22:25], v[70:73], v[50:53], v[22:25]
	v_mfma_f32_16x16x32_f16 v[42:45], v[62:65], v[54:57], v[42:45]
	v_mfma_f32_16x16x32_f16 v[34:37], v[70:73], v[54:57], v[34:37]
	v_mfma_f32_16x16x32_f16 v[10:13], v[62:65], v[58:61], v[10:13]
	v_mfma_f32_16x16x32_f16 v[18:21], v[70:73], v[58:61], v[18:21]
	s_waitcnt lgkmcnt(0)
	v_mfma_f32_16x16x32_f16 v[26:29], v[82:85], v[38:41], v[26:29]
	v_mfma_f32_16x16x32_f16 v[14:17], v[86:89], v[38:41], v[14:17]
	ds_read_b128 v[38:41], v0
	ds_read_b128 v[50:53], v0 offset:2048
	ds_read_b128 v[54:57], v0 offset:4096
	ds_read_b128 v[58:61], v0 offset:6144
	ds_read_b128 v[62:65], v4 offset:16384
	ds_read_b128 v[70:73], v4 offset:18432
	v_mfma_f32_16x16x32_f16 v[66:69], v[82:85], v[46:49], v[66:69]
	v_mfma_f32_16x16x32_f16 v[22:25], v[86:89], v[46:49], v[22:25]
	v_mfma_f32_16x16x32_f16 v[42:45], v[82:85], v[74:77], v[42:45]
	v_mfma_f32_16x16x32_f16 v[34:37], v[86:89], v[74:77], v[34:37]
	v_mfma_f32_16x16x32_f16 v[10:13], v[82:85], v[78:81], v[10:13]
	v_mfma_f32_16x16x32_f16 v[18:21], v[86:89], v[78:81], v[18:21]
	s_add_u32 s20, s0, 0x500
	s_mov_b32 m0, s18
	s_waitcnt vmcnt(0) lgkmcnt(0)
	s_barrier
	s_addc_u32 s21, s1, 0
	s_add_u32 s22, s4, 0x500
	global_load_lds_dwordx4 v1, s[20:21]
	s_mov_b32 m0, s15
	s_addc_u32 s23, s5, 0
	global_load_lds_dwordx4 v2, s[20:21]
	s_mov_b32 m0, s16
	s_nop 0
	global_load_lds_dwordx4 v1, s[22:23]
	s_mov_b32 m0, s17
	s_nop 0
	global_load_lds_dwordx4 v2, s[22:23]
	s_waitcnt lgkmcnt(0)
	v_mfma_f32_16x16x32_f16 v[26:29], v[62:65], v[38:41], v[26:29]
	v_mfma_f32_16x16x32_f16 v[14:17], v[70:73], v[38:41], v[14:17]
	ds_read_b128 v[38:41], v5 offset:32768
	ds_read_b128 v[46:49], v5 offset:34816
	ds_read_b128 v[74:77], v5 offset:36864
	ds_read_b128 v[78:81], v5 offset:38912
	ds_read_b128 v[82:85], v3 offset:49152
	ds_read_b128 v[86:89], v3 offset:51200
	v_mfma_f32_16x16x32_f16 v[66:69], v[62:65], v[50:53], v[66:69]
	v_mfma_f32_16x16x32_f16 v[22:25], v[70:73], v[50:53], v[22:25]
	v_mfma_f32_16x16x32_f16 v[42:45], v[62:65], v[54:57], v[42:45]
	v_mfma_f32_16x16x32_f16 v[34:37], v[70:73], v[54:57], v[34:37]
	v_mfma_f32_16x16x32_f16 v[10:13], v[62:65], v[58:61], v[10:13]
	v_mfma_f32_16x16x32_f16 v[18:21], v[70:73], v[58:61], v[18:21]
	s_waitcnt lgkmcnt(0)
	v_mfma_f32_16x16x32_f16 v[26:29], v[82:85], v[38:41], v[26:29]
	v_mfma_f32_16x16x32_f16 v[14:17], v[86:89], v[38:41], v[14:17]
	ds_read_b128 v[38:41], v0 offset:32768
	ds_read_b128 v[50:53], v0 offset:34816
	ds_read_b128 v[54:57], v0 offset:36864
	ds_read_b128 v[58:61], v0 offset:38912
	ds_read_b128 v[62:65], v4 offset:49152
	ds_read_b128 v[70:73], v4 offset:51200
	v_mfma_f32_16x16x32_f16 v[66:69], v[82:85], v[46:49], v[66:69]
	v_mfma_f32_16x16x32_f16 v[22:25], v[86:89], v[46:49], v[22:25]
	v_mfma_f32_16x16x32_f16 v[42:45], v[82:85], v[74:77], v[42:45]
	v_mfma_f32_16x16x32_f16 v[34:37], v[86:89], v[74:77], v[34:37]
	v_mfma_f32_16x16x32_f16 v[10:13], v[82:85], v[78:81], v[10:13]
	v_mfma_f32_16x16x32_f16 v[18:21], v[86:89], v[78:81], v[18:21]
	s_add_u32 s20, s0, 0x580
	s_mov_b32 m0, s14
	s_waitcnt vmcnt(0) lgkmcnt(0)
	s_barrier
	s_addc_u32 s21, s1, 0
	s_add_u32 s22, s4, 0x580
	global_load_lds_dwordx4 v1, s[20:21]
	s_mov_b32 m0, s3
	s_addc_u32 s23, s5, 0
	global_load_lds_dwordx4 v2, s[20:21]
	s_mov_b32 m0, s6
	s_nop 0
	global_load_lds_dwordx4 v1, s[22:23]
	s_mov_b32 m0, s7
	s_nop 0
	global_load_lds_dwordx4 v2, s[22:23]
	s_waitcnt lgkmcnt(0)
	v_mfma_f32_16x16x32_f16 v[26:29], v[62:65], v[38:41], v[26:29]
	v_mfma_f32_16x16x32_f16 v[14:17], v[70:73], v[38:41], v[14:17]
	ds_read_b128 v[38:41], v5
	ds_read_b128 v[46:49], v5 offset:2048
	ds_read_b128 v[74:77], v5 offset:4096
	ds_read_b128 v[78:81], v5 offset:6144
	ds_read_b128 v[82:85], v3 offset:16384
	ds_read_b128 v[86:89], v3 offset:18432
	v_mfma_f32_16x16x32_f16 v[66:69], v[62:65], v[50:53], v[66:69]
	v_mfma_f32_16x16x32_f16 v[22:25], v[70:73], v[50:53], v[22:25]
	v_mfma_f32_16x16x32_f16 v[42:45], v[62:65], v[54:57], v[42:45]
	v_mfma_f32_16x16x32_f16 v[34:37], v[70:73], v[54:57], v[34:37]
	v_mfma_f32_16x16x32_f16 v[10:13], v[62:65], v[58:61], v[10:13]
	v_mfma_f32_16x16x32_f16 v[18:21], v[70:73], v[58:61], v[18:21]
	s_waitcnt lgkmcnt(0)
	v_mfma_f32_16x16x32_f16 v[26:29], v[82:85], v[38:41], v[26:29]
	v_mfma_f32_16x16x32_f16 v[14:17], v[86:89], v[38:41], v[14:17]
	ds_read_b128 v[38:41], v0
	ds_read_b128 v[50:53], v0 offset:2048
	ds_read_b128 v[54:57], v0 offset:4096
	ds_read_b128 v[58:61], v0 offset:6144
	ds_read_b128 v[62:65], v4 offset:16384
	ds_read_b128 v[70:73], v4 offset:18432
	v_mfma_f32_16x16x32_f16 v[66:69], v[82:85], v[46:49], v[66:69]
	v_mfma_f32_16x16x32_f16 v[22:25], v[86:89], v[46:49], v[22:25]
	v_mfma_f32_16x16x32_f16 v[42:45], v[82:85], v[74:77], v[42:45]
	v_mfma_f32_16x16x32_f16 v[34:37], v[86:89], v[74:77], v[34:37]
	v_mfma_f32_16x16x32_f16 v[10:13], v[82:85], v[78:81], v[10:13]
	v_mfma_f32_16x16x32_f16 v[18:21], v[86:89], v[78:81], v[18:21]
	s_add_u32 s20, s0, 0x600
	s_mov_b32 m0, s18
	s_waitcnt vmcnt(0) lgkmcnt(0)
	s_barrier
	s_addc_u32 s21, s1, 0
	s_add_u32 s22, s4, 0x600
	global_load_lds_dwordx4 v1, s[20:21]
	s_mov_b32 m0, s15
	s_addc_u32 s23, s5, 0
	global_load_lds_dwordx4 v2, s[20:21]
	s_mov_b32 m0, s16
	s_nop 0
	global_load_lds_dwordx4 v1, s[22:23]
	s_mov_b32 m0, s17
	s_nop 0
	global_load_lds_dwordx4 v2, s[22:23]
	s_waitcnt lgkmcnt(0)
	v_mfma_f32_16x16x32_f16 v[26:29], v[62:65], v[38:41], v[26:29]
	v_mfma_f32_16x16x32_f16 v[14:17], v[70:73], v[38:41], v[14:17]
	ds_read_b128 v[38:41], v5 offset:32768
	ds_read_b128 v[46:49], v5 offset:34816
	ds_read_b128 v[74:77], v5 offset:36864
	ds_read_b128 v[78:81], v5 offset:38912
	ds_read_b128 v[82:85], v3 offset:49152
	ds_read_b128 v[86:89], v3 offset:51200
	v_mfma_f32_16x16x32_f16 v[66:69], v[62:65], v[50:53], v[66:69]
	v_mfma_f32_16x16x32_f16 v[22:25], v[70:73], v[50:53], v[22:25]
	v_mfma_f32_16x16x32_f16 v[42:45], v[62:65], v[54:57], v[42:45]
	v_mfma_f32_16x16x32_f16 v[34:37], v[70:73], v[54:57], v[34:37]
	v_mfma_f32_16x16x32_f16 v[10:13], v[62:65], v[58:61], v[10:13]
	v_mfma_f32_16x16x32_f16 v[18:21], v[70:73], v[58:61], v[18:21]
	s_waitcnt lgkmcnt(0)
	v_mfma_f32_16x16x32_f16 v[26:29], v[82:85], v[38:41], v[26:29]
	v_mfma_f32_16x16x32_f16 v[14:17], v[86:89], v[38:41], v[14:17]
	ds_read_b128 v[38:41], v0 offset:32768
	ds_read_b128 v[50:53], v0 offset:34816
	ds_read_b128 v[54:57], v0 offset:36864
	ds_read_b128 v[58:61], v0 offset:38912
	ds_read_b128 v[62:65], v4 offset:49152
	ds_read_b128 v[70:73], v4 offset:51200
	v_mfma_f32_16x16x32_f16 v[66:69], v[82:85], v[46:49], v[66:69]
	v_mfma_f32_16x16x32_f16 v[22:25], v[86:89], v[46:49], v[22:25]
	v_mfma_f32_16x16x32_f16 v[42:45], v[82:85], v[74:77], v[42:45]
	v_mfma_f32_16x16x32_f16 v[34:37], v[86:89], v[74:77], v[34:37]
	v_mfma_f32_16x16x32_f16 v[10:13], v[82:85], v[78:81], v[10:13]
	v_mfma_f32_16x16x32_f16 v[18:21], v[86:89], v[78:81], v[18:21]
	s_add_u32 s20, s0, 0x680
	s_mov_b32 m0, s14
	s_waitcnt vmcnt(0) lgkmcnt(0)
	s_barrier
	s_addc_u32 s21, s1, 0
	s_add_u32 s22, s4, 0x680
	global_load_lds_dwordx4 v1, s[20:21]
	s_mov_b32 m0, s3
	s_addc_u32 s23, s5, 0
	global_load_lds_dwordx4 v2, s[20:21]
	s_mov_b32 m0, s6
	s_nop 0
	global_load_lds_dwordx4 v1, s[22:23]
	s_mov_b32 m0, s7
	s_nop 0
	global_load_lds_dwordx4 v2, s[22:23]
	s_waitcnt lgkmcnt(0)
	v_mfma_f32_16x16x32_f16 v[26:29], v[62:65], v[38:41], v[26:29]
	v_mfma_f32_16x16x32_f16 v[14:17], v[70:73], v[38:41], v[14:17]
	ds_read_b128 v[38:41], v5
	ds_read_b128 v[46:49], v5 offset:2048
	ds_read_b128 v[74:77], v5 offset:4096
	ds_read_b128 v[78:81], v5 offset:6144
	ds_read_b128 v[82:85], v3 offset:16384
	ds_read_b128 v[86:89], v3 offset:18432
	v_mfma_f32_16x16x32_f16 v[66:69], v[62:65], v[50:53], v[66:69]
	v_mfma_f32_16x16x32_f16 v[22:25], v[70:73], v[50:53], v[22:25]
	v_mfma_f32_16x16x32_f16 v[42:45], v[62:65], v[54:57], v[42:45]
	v_mfma_f32_16x16x32_f16 v[34:37], v[70:73], v[54:57], v[34:37]
	v_mfma_f32_16x16x32_f16 v[10:13], v[62:65], v[58:61], v[10:13]
	v_mfma_f32_16x16x32_f16 v[18:21], v[70:73], v[58:61], v[18:21]
	s_waitcnt lgkmcnt(0)
	v_mfma_f32_16x16x32_f16 v[26:29], v[82:85], v[38:41], v[26:29]
	v_mfma_f32_16x16x32_f16 v[14:17], v[86:89], v[38:41], v[14:17]
	ds_read_b128 v[38:41], v0
	ds_read_b128 v[50:53], v0 offset:2048
	ds_read_b128 v[54:57], v0 offset:4096
	ds_read_b128 v[58:61], v0 offset:6144
	ds_read_b128 v[62:65], v4 offset:16384
	ds_read_b128 v[70:73], v4 offset:18432
	v_mfma_f32_16x16x32_f16 v[66:69], v[82:85], v[46:49], v[66:69]
	v_mfma_f32_16x16x32_f16 v[22:25], v[86:89], v[46:49], v[22:25]
	v_mfma_f32_16x16x32_f16 v[42:45], v[82:85], v[74:77], v[42:45]
	v_mfma_f32_16x16x32_f16 v[34:37], v[86:89], v[74:77], v[34:37]
	v_mfma_f32_16x16x32_f16 v[10:13], v[82:85], v[78:81], v[10:13]
	v_mfma_f32_16x16x32_f16 v[18:21], v[86:89], v[78:81], v[18:21]
	s_mov_b32 m0, s18
	s_add_u32 s18, s0, 0x700
	s_waitcnt vmcnt(0) lgkmcnt(0)
	s_barrier
	s_addc_u32 s19, s1, 0
	s_add_u32 s20, s4, 0x700
	global_load_lds_dwordx4 v1, s[18:19]
	s_mov_b32 m0, s15
	s_addc_u32 s21, s5, 0
	global_load_lds_dwordx4 v2, s[18:19]
	s_mov_b32 m0, s16
	s_nop 0
	global_load_lds_dwordx4 v1, s[20:21]
	s_mov_b32 m0, s17
	s_nop 0
	global_load_lds_dwordx4 v2, s[20:21]
	s_waitcnt lgkmcnt(0)
	v_mfma_f32_16x16x32_f16 v[26:29], v[62:65], v[38:41], v[26:29]
	v_mfma_f32_16x16x32_f16 v[14:17], v[70:73], v[38:41], v[14:17]
	ds_read_b128 v[38:41], v5 offset:32768
	ds_read_b128 v[46:49], v5 offset:34816
	ds_read_b128 v[74:77], v5 offset:36864
	ds_read_b128 v[78:81], v5 offset:38912
	ds_read_b128 v[82:85], v3 offset:49152
	ds_read_b128 v[86:89], v3 offset:51200
	v_mfma_f32_16x16x32_f16 v[66:69], v[62:65], v[50:53], v[66:69]
	v_mfma_f32_16x16x32_f16 v[22:25], v[70:73], v[50:53], v[22:25]
	v_mfma_f32_16x16x32_f16 v[42:45], v[62:65], v[54:57], v[42:45]
	v_mfma_f32_16x16x32_f16 v[34:37], v[70:73], v[54:57], v[34:37]
	v_mfma_f32_16x16x32_f16 v[10:13], v[62:65], v[58:61], v[10:13]
	v_mfma_f32_16x16x32_f16 v[18:21], v[70:73], v[58:61], v[18:21]
	s_waitcnt lgkmcnt(0)
	v_mfma_f32_16x16x32_f16 v[26:29], v[82:85], v[38:41], v[26:29]
	v_mfma_f32_16x16x32_f16 v[14:17], v[86:89], v[38:41], v[14:17]
	ds_read_b128 v[38:41], v0 offset:32768
	ds_read_b128 v[50:53], v0 offset:34816
	ds_read_b128 v[54:57], v0 offset:36864
	ds_read_b128 v[58:61], v0 offset:38912
	ds_read_b128 v[62:65], v4 offset:49152
	ds_read_b128 v[70:73], v4 offset:51200
	v_mfma_f32_16x16x32_f16 v[66:69], v[82:85], v[46:49], v[66:69]
	v_mfma_f32_16x16x32_f16 v[22:25], v[86:89], v[46:49], v[22:25]
	v_mfma_f32_16x16x32_f16 v[42:45], v[82:85], v[74:77], v[42:45]
	v_mfma_f32_16x16x32_f16 v[34:37], v[86:89], v[74:77], v[34:37]
	v_mfma_f32_16x16x32_f16 v[10:13], v[82:85], v[78:81], v[10:13]
	v_mfma_f32_16x16x32_f16 v[18:21], v[86:89], v[78:81], v[18:21]
	s_add_u32 s0, s0, 0x780
	s_mov_b32 m0, s14
	s_waitcnt vmcnt(0) lgkmcnt(0)
	s_barrier
	s_addc_u32 s1, s1, 0
	s_add_u32 s4, s4, 0x780
	global_load_lds_dwordx4 v1, s[0:1]
	s_mov_b32 m0, s3
	s_addc_u32 s5, s5, 0
	global_load_lds_dwordx4 v2, s[0:1]
	s_mov_b32 m0, s6
	s_nop 0
	global_load_lds_dwordx4 v1, s[4:5]
	s_mov_b32 m0, s7
	s_nop 0
	global_load_lds_dwordx4 v2, s[4:5]
	s_waitcnt lgkmcnt(0)
	v_mfma_f32_16x16x32_f16 v[26:29], v[62:65], v[38:41], v[26:29]
	v_mfma_f32_16x16x32_f16 v[14:17], v[70:73], v[38:41], v[14:17]
	ds_read_b128 v[38:41], v5
	ds_read_b128 v[46:49], v5 offset:2048
	ds_read_b128 v[74:77], v5 offset:4096
	ds_read_b128 v[78:81], v5 offset:6144
	ds_read_b128 v[82:85], v3 offset:16384
	ds_read_b128 v[86:89], v3 offset:18432
	v_mfma_f32_16x16x32_f16 v[66:69], v[62:65], v[50:53], v[66:69]
	v_mfma_f32_16x16x32_f16 v[22:25], v[70:73], v[50:53], v[22:25]
	v_mfma_f32_16x16x32_f16 v[42:45], v[62:65], v[54:57], v[42:45]
	v_mfma_f32_16x16x32_f16 v[34:37], v[70:73], v[54:57], v[34:37]
	v_mfma_f32_16x16x32_f16 v[10:13], v[62:65], v[58:61], v[10:13]
	v_mfma_f32_16x16x32_f16 v[18:21], v[70:73], v[58:61], v[18:21]
	s_waitcnt lgkmcnt(0)
	v_mfma_f32_16x16x32_f16 v[26:29], v[82:85], v[38:41], v[26:29]
	v_mfma_f32_16x16x32_f16 v[14:17], v[86:89], v[38:41], v[14:17]
	ds_read_b128 v[38:41], v0
	ds_read_b128 v[50:53], v0 offset:2048
	ds_read_b128 v[54:57], v0 offset:4096
	ds_read_b128 v[58:61], v0 offset:6144
	ds_read_b128 v[62:65], v4 offset:16384
	ds_read_b128 v[70:73], v4 offset:18432
	v_mfma_f32_16x16x32_f16 v[66:69], v[82:85], v[46:49], v[66:69]
	v_mfma_f32_16x16x32_f16 v[22:25], v[86:89], v[46:49], v[22:25]
	v_mfma_f32_16x16x32_f16 v[42:45], v[82:85], v[74:77], v[42:45]
	v_mfma_f32_16x16x32_f16 v[34:37], v[86:89], v[74:77], v[34:37]
	v_mfma_f32_16x16x32_f16 v[10:13], v[82:85], v[78:81], v[10:13]
	v_mfma_f32_16x16x32_f16 v[18:21], v[86:89], v[78:81], v[18:21]
	s_waitcnt vmcnt(0) lgkmcnt(0)
	s_barrier
	s_waitcnt lgkmcnt(0)
	v_mfma_f32_16x16x32_f16 v[26:29], v[62:65], v[38:41], v[26:29]
	v_mfma_f32_16x16x32_f16 v[14:17], v[70:73], v[38:41], v[14:17]
	ds_read_b128 v[38:41], v5 offset:32768
	ds_read_b128 v[46:49], v5 offset:34816
	ds_read_b128 v[74:77], v5 offset:36864
	ds_read_b128 v[78:81], v5 offset:38912
	ds_read_b128 v[82:85], v3 offset:49152
	ds_read_b128 v[86:89], v3 offset:51200
	v_mfma_f32_16x16x32_f16 v[66:69], v[62:65], v[50:53], v[66:69]
	v_mfma_f32_16x16x32_f16 v[22:25], v[70:73], v[50:53], v[22:25]
	v_mfma_f32_16x16x32_f16 v[42:45], v[62:65], v[54:57], v[42:45]
	v_mfma_f32_16x16x32_f16 v[34:37], v[70:73], v[54:57], v[34:37]
	v_mfma_f32_16x16x32_f16 v[10:13], v[62:65], v[58:61], v[10:13]
	v_mfma_f32_16x16x32_f16 v[18:21], v[70:73], v[58:61], v[18:21]
	s_waitcnt lgkmcnt(0)
	v_mfma_f32_16x16x32_f16 v[26:29], v[82:85], v[38:41], v[26:29]
	v_mfma_f32_16x16x32_f16 v[14:17], v[86:89], v[38:41], v[14:17]
	ds_read_b128 v[38:41], v0 offset:32768
	ds_read_b128 v[50:53], v0 offset:34816
	ds_read_b128 v[54:57], v0 offset:36864
	ds_read_b128 v[0:3], v0 offset:38912
	ds_read_b128 v[58:61], v4 offset:49152
	ds_read_b128 v[62:65], v4 offset:51200
	v_mfma_f32_16x16x32_f16 v[4:7], v[82:85], v[46:49], v[66:69]
	v_mfma_f32_16x16x32_f16 v[22:25], v[86:89], v[46:49], v[22:25]
	v_mfma_f32_16x16x32_f16 v[42:45], v[82:85], v[74:77], v[42:45]
	v_mfma_f32_16x16x32_f16 v[34:37], v[86:89], v[74:77], v[34:37]
	v_mfma_f32_16x16x32_f16 v[10:13], v[82:85], v[78:81], v[10:13]
	v_mfma_f32_16x16x32_f16 v[46:49], v[86:89], v[78:81], v[18:21]
	s_waitcnt lgkmcnt(0)
	v_mfma_f32_16x16x32_f16 v[66:69], v[58:61], v[38:41], v[26:29]
	v_mfma_f32_16x16x32_f16 v[38:41], v[62:65], v[38:41], v[14:17]
	v_mfma_f32_16x16x32_f16 v[28:31], v[58:61], v[50:53], v[4:7]
	v_mfma_f32_16x16x32_f16 v[24:27], v[62:65], v[50:53], v[22:25]
	v_mfma_f32_16x16x32_f16 v[20:23], v[58:61], v[54:57], v[42:45]
	v_mfma_f32_16x16x32_f16 v[16:19], v[62:65], v[54:57], v[34:37]
	v_mfma_f32_16x16x32_f16 v[4:7], v[58:61], v[0:3], v[10:13]
	v_mfma_f32_16x16x32_f16 v[0:3], v[62:65], v[0:3], v[46:49]
	s_barrier
	v_mul_u32_u24_e32 v92, 0x110, v32
	v_and_b32_e32 v93, 15, v32
	v_lshrrev_b32_e32 v94, 6, v32
	v_lshrrev_b32_e32 v95, 5, v8
	v_lshl_add_u32 v92, v8, 1, v92
	v_lshl_or_b32 v93, v9, 4, v93
	v_lshl_or_b32 v94, v94, 2, v95
	v_lshl_add_u32 v92, v9, 3, v92
	v_lshl_or_b32 v93, v94, 6, v93
	v_lshrrev_b32_e32 v95, 4, v93
	v_and_b32_e32 v93, 15, v93
	v_mul_u32_u24_e32 v94, 0x110, v95
	v_lshlrev_b32_e32 v95, 13, v95
	v_lshl_add_u32 v94, v93, 4, v94
	v_lshl_add_u32 v95, v93, 4, v95
	s_lshl_b32 s26, s12, 13
	s_lshl_b32 s27, s13, 1
	s_add_u32 s26, s26, s27
	s_add_u32 s24, s8, s26
	s_addc_u32 s25, s9, 0
	s_add_u32 s26, s24, 0x40000
	s_addc_u32 s27, s25, 0
	s_add_u32 s28, s26, 0x40000
	s_addc_u32 s29, s27, 0
	s_add_u32 s30, s28, 0x40000
	s_addc_u32 s31, s29, 0
	v_lshlrev_b32_e32 v9, 2, v9
	v_or3_b32 v34, v9, v8, s13
	v_mov_b32_e32 v35, 0
	v_lshl_add_u64 v[36:37], v[34:35], 2, s[10:11]
	global_load_dwordx4 v[8:11], v[36:37], off
	global_load_dwordx4 v[12:15], v[36:37], off offset:64
	v_or_b32_e32 v36, s12, v32
	v_mad_u64_u32 v[42:43], s[18:19], v36, s2, 0
	s_ashr_i32 s1, s2, 31
	s_mov_b32 s16, 0xbf3a00e3
	v_mov_b32_e32 v44, v43
	v_mov_b64_e32 v[32:33], s[16:17]
	v_mad_u64_u32 v[44:45], s[16:17], v36, s1, v[44:45]
	s_mov_b32 s14, 0x3e6d3388
	v_mov_b32_e32 v43, v44
	s_mov_b32 s10, 0x3f07dc22
	s_mov_b32 s6, 0xbf38aa3b
	s_mov_b32 s12, 0x3f35f0e3
	s_mov_b32 s0, 0xbe11a98e
	s_mov_b32 s4, 0x3e027906
	v_lshlrev_b64 v[34:35], 1, v[34:35]
	v_lshl_add_u64 v[42:43], v[42:43], 1, s[8:9]
	v_lshl_add_u64 v[42:43], v[42:43], 0, v[34:35]
	s_waitcnt vmcnt(0)
	v_pk_add_f32 v[46:47], v[66:67], v[8:9]
	v_pk_add_f32 v[44:45], v[68:69], v[10:11]
	v_and_b32_e32 v49, 0x7fffffff, v47
	v_and_b32_e32 v48, 0x7fffffff, v46
	v_and_b32_e32 v55, 0x7fffffff, v45
	v_and_b32_e32 v54, 0x7fffffff, v44
	v_pk_fma_f32 v[48:49], v[48:49], s[14:15], 1.0 op_sel_hi:[1,0,0]
	v_pk_add_f32 v[38:39], v[38:39], v[12:13]
	v_pk_fma_f32 v[54:55], v[54:55], s[14:15], 1.0 op_sel_hi:[1,0,0]
	v_rcp_f32_e32 v48, v48
	v_rcp_f32_e32 v49, v49
	v_and_b32_e32 v57, 0x7fffffff, v39
	v_and_b32_e32 v56, 0x7fffffff, v38
	v_rcp_f32_e32 v54, v54
	v_rcp_f32_e32 v55, v55
	v_pk_fma_f32 v[56:57], v[56:57], s[14:15], 1.0 op_sel_hi:[1,0,0]
	v_pk_mul_f32 v[52:53], v[46:47], v[46:47]
	v_rcp_f32_e32 v56, v56
	v_rcp_f32_e32 v57, v57
	v_pk_mul_f32 v[50:51], v[44:45], v[44:45]
	v_pk_mul_f32 v[52:53], v[52:53], s[6:7] op_sel_hi:[1,0]
	v_pk_fma_f32 v[64:65], v[48:49], s[10:11], v[32:33] op_sel_hi:[1,0,0]
	v_pk_mul_f32 v[50:51], v[50:51], s[6:7] op_sel_hi:[1,0]
	v_exp_f32_e32 v52, v52
	v_exp_f32_e32 v53, v53
	v_pk_fma_f32 v[66:67], v[54:55], s[10:11], v[32:33] op_sel_hi:[1,0,0]
	v_pk_fma_f32 v[64:65], v[48:49], v[64:65], s[12:13] op_sel_hi:[1,1,0]
	v_pk_mul_f32 v[60:61], v[38:39], v[38:39]
	v_exp_f32_e32 v50, v50
	v_exp_f32_e32 v51, v51
	v_pk_fma_f32 v[66:67], v[54:55], v[66:67], s[12:13] op_sel_hi:[1,1,0]
	v_pk_fma_f32 v[64:65], v[48:49], v[64:65], s[0:1] op_sel_hi:[1,1,0]
	v_pk_mul_f32 v[60:61], v[60:61], s[6:7] op_sel_hi:[1,0]
	v_pk_fma_f32 v[68:69], v[56:57], s[10:11], v[32:33] op_sel_hi:[1,0,0]
	v_pk_fma_f32 v[66:67], v[54:55], v[66:67], s[0:1] op_sel_hi:[1,1,0]
	v_pk_fma_f32 v[64:65], v[48:49], v[64:65], s[4:5] op_sel_hi:[1,1,0]
	v_exp_f32_e32 v60, v60
	v_exp_f32_e32 v61, v61
	v_pk_fma_f32 v[68:69], v[56:57], v[68:69], s[12:13] op_sel_hi:[1,1,0]
	v_pk_fma_f32 v[66:67], v[54:55], v[66:67], s[4:5] op_sel_hi:[1,1,0]
	v_pk_mul_f32 v[48:49], v[48:49], v[64:65]
	v_pk_add_f32 v[40:41], v[40:41], v[14:15]
	v_pk_fma_f32 v[68:69], v[56:57], v[68:69], s[0:1] op_sel_hi:[1,1,0]
	v_pk_mul_f32 v[54:55], v[54:55], v[66:67]
	v_pk_mul_f32 v[48:49], v[52:53], v[48:49]
	v_and_b32_e32 v63, 0x7fffffff, v41
	v_and_b32_e32 v62, 0x7fffffff, v40
	v_pk_fma_f32 v[68:69], v[56:57], v[68:69], s[4:5] op_sel_hi:[1,1,0]
	v_pk_mul_f32 v[50:51], v[50:51], v[54:55]
	v_pk_mul_f32 v[54:55], v[46:47], v[48:49]
	v_pk_fma_f32 v[48:49], v[46:47], v[48:49], v[46:47] neg_lo:[1,0,0] neg_hi:[1,0,0]
	v_cmp_gt_f32_e32 vcc, 0, v46
	v_pk_fma_f32 v[62:63], v[62:63], s[14:15], 1.0 op_sel_hi:[1,0,0]
	v_pk_mul_f32 v[56:57], v[56:57], v[68:69]
	v_cndmask_b32_e32 v37, v48, v54, vcc
	v_cmp_gt_f32_e32 vcc, 0, v47
	v_rcp_f32_e32 v62, v62
	v_rcp_f32_e32 v63, v63
	v_pk_mul_f32 v[52:53], v[60:61], v[56:57]
	v_pk_mul_f32 v[56:57], v[44:45], v[50:51]
	v_pk_fma_f32 v[50:51], v[44:45], v[50:51], v[44:45] neg_lo:[1,0,0] neg_hi:[1,0,0]
	v_cndmask_b32_e32 v46, v49, v55, vcc
	v_cmp_gt_f32_e32 vcc, 0, v44
	v_pk_mul_f32 v[58:59], v[40:41], v[40:41]
	v_pk_mul_f32 v[60:61], v[38:39], v[52:53]
	v_cndmask_b32_e32 v44, v50, v56, vcc
	v_cmp_gt_f32_e32 vcc, 0, v45
	v_pk_fma_f32 v[52:53], v[38:39], v[52:53], v[38:39] neg_lo:[1,0,0] neg_hi:[1,0,0]
	v_pk_add_f32 v[28:29], v[28:29], v[8:9]
	v_cndmask_b32_e32 v45, v51, v57, vcc
	v_cmp_gt_f32_e32 vcc, 0, v38
	v_cvt_pk_f16_f32 v45, v44, v45
	v_cvt_pk_f16_f32 v44, v37, v46
	v_cndmask_b32_e32 v47, v52, v60, vcc
	ds_write_b64 v92, v[44:45]
	v_cmp_gt_f32_e32 vcc, 0, v39
	v_pk_fma_f32 v[38:39], v[62:63], s[10:11], v[32:33] op_sel_hi:[1,0,0]
	v_pk_mul_f32 v[44:45], v[58:59], s[6:7] op_sel_hi:[1,0]
	v_pk_fma_f32 v[38:39], v[62:63], v[38:39], s[12:13] op_sel_hi:[1,1,0]
	v_exp_f32_e32 v44, v44
	v_exp_f32_e32 v45, v45
	v_pk_fma_f32 v[38:39], v[62:63], v[38:39], s[0:1] op_sel_hi:[1,1,0]
	v_cndmask_b32_e32 v37, v53, v61, vcc
	v_pk_fma_f32 v[38:39], v[62:63], v[38:39], s[4:5] op_sel_hi:[1,1,0]
	v_cmp_gt_f32_e32 vcc, 0, v40
	v_pk_mul_f32 v[38:39], v[62:63], v[38:39]
	v_pk_add_f32 v[30:31], v[30:31], v[10:11]
	v_pk_mul_f32 v[38:39], v[44:45], v[38:39]
	v_and_b32_e32 v46, 0x7fffffff, v30
	v_pk_mul_f32 v[44:45], v[40:41], v[38:39]
	v_pk_fma_f32 v[38:39], v[40:41], v[38:39], v[40:41] neg_lo:[1,0,0] neg_hi:[1,0,0]
	v_pk_add_f32 v[24:25], v[24:25], v[12:13]
	v_cndmask_b32_e32 v38, v38, v44, vcc
	v_cmp_gt_f32_e32 vcc, 0, v41
	v_pk_add_f32 v[26:27], v[26:27], v[14:15]
	v_pk_add_f32 v[20:21], v[20:21], v[8:9]
	v_cndmask_b32_e32 v39, v39, v45, vcc
	v_cvt_pk_f16_f32 v39, v38, v39
	v_cvt_pk_f16_f32 v38, v47, v37
	ds_write_b64 v92, v[38:39] offset:32
	v_and_b32_e32 v43, 0x7fffffff, v29
	v_and_b32_e32 v42, 0x7fffffff, v28
	v_pk_fma_f32 v[42:43], v[42:43], s[14:15], 1.0 op_sel_hi:[1,0,0]
	v_or_b32_e32 v37, 16, v36
	v_rcp_f32_e32 v42, v42
	v_rcp_f32_e32 v43, v43
	v_mad_u64_u32 v[38:39], s[16:17], v37, s2, 0
	v_mov_b32_e32 v40, v39
	v_mad_u64_u32 v[40:41], s[16:17], v37, s1, v[40:41]
	v_pk_mul_f32 v[44:45], v[28:29], v[28:29]
	v_mov_b32_e32 v39, v40
	v_pk_fma_f32 v[40:41], v[42:43], s[10:11], v[32:33] op_sel_hi:[1,0,0]
	v_pk_mul_f32 v[44:45], v[44:45], s[6:7] op_sel_hi:[1,0]
	v_pk_fma_f32 v[40:41], v[42:43], v[40:41], s[12:13] op_sel_hi:[1,1,0]
	v_exp_f32_e32 v44, v44
	v_exp_f32_e32 v45, v45
	v_pk_fma_f32 v[40:41], v[42:43], v[40:41], s[0:1] op_sel_hi:[1,1,0]
	v_and_b32_e32 v47, 0x7fffffff, v31
	v_pk_fma_f32 v[40:41], v[42:43], v[40:41], s[4:5] op_sel_hi:[1,1,0]
	v_pk_fma_f32 v[46:47], v[46:47], s[14:15], 1.0 op_sel_hi:[1,0,0]
	v_pk_mul_f32 v[40:41], v[42:43], v[40:41]
	v_rcp_f32_e32 v46, v46
	v_rcp_f32_e32 v47, v47
	v_pk_mul_f32 v[40:41], v[44:45], v[40:41]
	v_cmp_gt_f32_e32 vcc, 0, v28
	v_pk_mul_f32 v[44:45], v[28:29], v[40:41]
	v_pk_fma_f32 v[40:41], v[28:29], v[40:41], v[28:29] neg_lo:[1,0,0] neg_hi:[1,0,0]
	v_pk_mul_f32 v[42:43], v[30:31], v[30:31]
	v_cndmask_b32_e32 v37, v40, v44, vcc
	v_cmp_gt_f32_e32 vcc, 0, v29
	v_pk_fma_f32 v[28:29], v[46:47], s[10:11], v[32:33] op_sel_hi:[1,0,0]
	v_lshl_add_u64 v[38:39], v[38:39], 1, s[8:9]
	v_cndmask_b32_e32 v44, v41, v45, vcc
	v_pk_mul_f32 v[40:41], v[42:43], s[6:7] op_sel_hi:[1,0]
	v_pk_fma_f32 v[28:29], v[46:47], v[28:29], s[12:13] op_sel_hi:[1,1,0]
	v_exp_f32_e32 v40, v40
	v_exp_f32_e32 v41, v41
	v_pk_fma_f32 v[28:29], v[46:47], v[28:29], s[0:1] op_sel_hi:[1,1,0]
	v_cmp_gt_f32_e32 vcc, 0, v30
	v_pk_fma_f32 v[28:29], v[46:47], v[28:29], s[4:5] op_sel_hi:[1,1,0]
	v_lshl_add_u64 v[38:39], v[38:39], 0, v[34:35]
	v_pk_mul_f32 v[28:29], v[46:47], v[28:29]
	v_and_b32_e32 v43, 0x7fffffff, v27
	v_pk_mul_f32 v[28:29], v[40:41], v[28:29]
	v_and_b32_e32 v42, 0x7fffffff, v26
	v_pk_mul_f32 v[40:41], v[30:31], v[28:29]
	v_pk_fma_f32 v[28:29], v[30:31], v[28:29], v[30:31] neg_lo:[1,0,0] neg_hi:[1,0,0]
	v_and_b32_e32 v30, 0x7fffffff, v24
	v_cndmask_b32_e32 v28, v28, v40, vcc
	v_cmp_gt_f32_e32 vcc, 0, v31
	v_and_b32_e32 v31, 0x7fffffff, v25
	v_pk_fma_f32 v[30:31], v[30:31], s[14:15], 1.0 op_sel_hi:[1,0,0]
	v_cndmask_b32_e32 v29, v29, v41, vcc
	v_rcp_f32_e32 v30, v30
	v_rcp_f32_e32 v31, v31
	v_cvt_pk_f16_f32 v29, v28, v29
	v_cvt_pk_f16_f32 v28, v37, v44
	v_pk_mul_f32 v[40:41], v[24:25], v[24:25]
	ds_write_b64 v92, v[28:29] offset:4352
	v_pk_fma_f32 v[28:29], v[30:31], s[10:11], v[32:33] op_sel_hi:[1,0,0]
	v_pk_mul_f32 v[40:41], v[40:41], s[6:7] op_sel_hi:[1,0]
	v_pk_fma_f32 v[28:29], v[30:31], v[28:29], s[12:13] op_sel_hi:[1,1,0]
	v_exp_f32_e32 v40, v40
	v_exp_f32_e32 v41, v41
	v_pk_fma_f32 v[28:29], v[30:31], v[28:29], s[0:1] op_sel_hi:[1,1,0]
	v_pk_fma_f32 v[42:43], v[42:43], s[14:15], 1.0 op_sel_hi:[1,0,0]
	v_pk_fma_f32 v[28:29], v[30:31], v[28:29], s[4:5] op_sel_hi:[1,1,0]
	v_rcp_f32_e32 v42, v42
	v_pk_mul_f32 v[28:29], v[30:31], v[28:29]
	v_rcp_f32_e32 v43, v43
	v_pk_mul_f32 v[28:29], v[40:41], v[28:29]
	v_cmp_gt_f32_e32 vcc, 0, v24
	v_pk_mul_f32 v[40:41], v[24:25], v[28:29]
	v_pk_fma_f32 v[28:29], v[24:25], v[28:29], v[24:25] neg_lo:[1,0,0] neg_hi:[1,0,0]
	v_pk_mul_f32 v[30:31], v[26:27], v[26:27]
	v_cndmask_b32_e32 v37, v28, v40, vcc
	v_cmp_gt_f32_e32 vcc, 0, v25
	v_pk_fma_f32 v[24:25], v[42:43], s[10:11], v[32:33] op_sel_hi:[1,0,0]
	v_pk_add_f32 v[22:23], v[22:23], v[10:11]
	v_cndmask_b32_e32 v40, v29, v41, vcc
	v_pk_mul_f32 v[28:29], v[30:31], s[6:7] op_sel_hi:[1,0]
	v_pk_fma_f32 v[24:25], v[42:43], v[24:25], s[12:13] op_sel_hi:[1,1,0]
	v_exp_f32_e32 v28, v28
	v_exp_f32_e32 v29, v29
	v_pk_fma_f32 v[24:25], v[42:43], v[24:25], s[0:1] op_sel_hi:[1,1,0]
	v_cmp_gt_f32_e32 vcc, 0, v26
	v_pk_fma_f32 v[24:25], v[42:43], v[24:25], s[4:5] op_sel_hi:[1,1,0]
	v_pk_mul_f32 v[30:31], v[20:21], v[20:21]
	v_pk_mul_f32 v[24:25], v[42:43], v[24:25]
	v_pk_mul_f32 v[30:31], v[30:31], s[6:7] op_sel_hi:[1,0]
	v_pk_mul_f32 v[24:25], v[28:29], v[24:25]
	v_exp_f32_e32 v30, v30
	v_pk_mul_f32 v[28:29], v[26:27], v[24:25]
	v_pk_fma_f32 v[24:25], v[26:27], v[24:25], v[26:27] neg_lo:[1,0,0] neg_hi:[1,0,0]
	v_exp_f32_e32 v31, v31
	v_cndmask_b32_e32 v24, v24, v28, vcc
	v_cmp_gt_f32_e32 vcc, 0, v27
	v_and_b32_e32 v28, 0x7fffffff, v20
	v_or_b32_e32 v27, 32, v36
	v_cndmask_b32_e32 v25, v25, v29, vcc
	v_and_b32_e32 v29, 0x7fffffff, v21
	v_pk_fma_f32 v[28:29], v[28:29], s[14:15], 1.0 op_sel_hi:[1,0,0]
	v_cvt_pk_f16_f32 v25, v24, v25
	v_cvt_pk_f16_f32 v24, v37, v40
	v_rcp_f32_e32 v28, v28
	v_rcp_f32_e32 v29, v29
	ds_write_b64 v92, v[24:25] offset:4384
	v_mad_u64_u32 v[24:25], s[16:17], v27, s2, 0
	v_mov_b32_e32 v26, v25
	v_mad_u64_u32 v[26:27], s[16:17], v27, s1, v[26:27]
	v_mov_b32_e32 v25, v26
	v_pk_fma_f32 v[26:27], v[28:29], s[10:11], v[32:33] op_sel_hi:[1,0,0]
	v_and_b32_e32 v39, 0x7fffffff, v23
	v_pk_fma_f32 v[26:27], v[28:29], v[26:27], s[12:13] op_sel_hi:[1,1,0]
	v_and_b32_e32 v38, 0x7fffffff, v22
	v_pk_fma_f32 v[26:27], v[28:29], v[26:27], s[0:1] op_sel_hi:[1,1,0]
	v_pk_fma_f32 v[38:39], v[38:39], s[14:15], 1.0 op_sel_hi:[1,0,0]
	v_pk_fma_f32 v[26:27], v[28:29], v[26:27], s[4:5] op_sel_hi:[1,1,0]
	v_rcp_f32_e32 v38, v38
	v_pk_mul_f32 v[26:27], v[28:29], v[26:27]
	v_rcp_f32_e32 v39, v39
	v_pk_mul_f32 v[26:27], v[30:31], v[26:27]
	v_cmp_gt_f32_e32 vcc, 0, v20
	v_pk_mul_f32 v[30:31], v[20:21], v[26:27]
	v_pk_fma_f32 v[26:27], v[20:21], v[26:27], v[20:21] neg_lo:[1,0,0] neg_hi:[1,0,0]
	v_pk_mul_f32 v[28:29], v[22:23], v[22:23]
	v_cndmask_b32_e32 v30, v26, v30, vcc
	v_cmp_gt_f32_e32 vcc, 0, v21
	v_pk_fma_f32 v[20:21], v[38:39], s[10:11], v[32:33] op_sel_hi:[1,0,0]
	v_pk_add_f32 v[16:17], v[16:17], v[12:13]
	v_cndmask_b32_e32 v31, v27, v31, vcc
	v_pk_mul_f32 v[26:27], v[28:29], s[6:7] op_sel_hi:[1,0]
	v_pk_fma_f32 v[20:21], v[38:39], v[20:21], s[12:13] op_sel_hi:[1,1,0]
	v_exp_f32_e32 v26, v26
	v_exp_f32_e32 v27, v27
	v_pk_fma_f32 v[20:21], v[38:39], v[20:21], s[0:1] op_sel_hi:[1,1,0]
	v_cmp_gt_f32_e32 vcc, 0, v22
	v_pk_fma_f32 v[20:21], v[38:39], v[20:21], s[4:5] op_sel_hi:[1,1,0]
	v_lshl_add_u64 v[24:25], v[24:25], 1, s[8:9]
	v_pk_mul_f32 v[20:21], v[38:39], v[20:21]
	v_lshl_add_u64 v[24:25], v[24:25], 0, v[34:35]
	v_pk_mul_f32 v[20:21], v[26:27], v[20:21]
	v_pk_add_f32 v[18:19], v[18:19], v[14:15]
	v_pk_mul_f32 v[26:27], v[22:23], v[20:21]
	v_pk_fma_f32 v[20:21], v[22:23], v[20:21], v[22:23] neg_lo:[1,0,0] neg_hi:[1,0,0]
	v_and_b32_e32 v22, 0x7fffffff, v16
	v_cndmask_b32_e32 v20, v20, v26, vcc
	v_cmp_gt_f32_e32 vcc, 0, v23
	v_and_b32_e32 v23, 0x7fffffff, v17
	v_pk_fma_f32 v[22:23], v[22:23], s[14:15], 1.0 op_sel_hi:[1,0,0]
	v_cndmask_b32_e32 v21, v21, v27, vcc
	v_rcp_f32_e32 v22, v22
	v_rcp_f32_e32 v23, v23
	v_cvt_pk_f16_f32 v21, v20, v21
	v_cvt_pk_f16_f32 v20, v30, v31
	v_pk_mul_f32 v[26:27], v[16:17], v[16:17]
	ds_write_b64 v92, v[20:21] offset:8704
	v_pk_fma_f32 v[20:21], v[22:23], s[10:11], v[32:33] op_sel_hi:[1,0,0]
	v_pk_mul_f32 v[26:27], v[26:27], s[6:7] op_sel_hi:[1,0]
	v_pk_fma_f32 v[20:21], v[22:23], v[20:21], s[12:13] op_sel_hi:[1,1,0]
	v_exp_f32_e32 v26, v26
	v_exp_f32_e32 v27, v27
	v_pk_fma_f32 v[20:21], v[22:23], v[20:21], s[0:1] op_sel_hi:[1,1,0]
	v_and_b32_e32 v29, 0x7fffffff, v19
	v_and_b32_e32 v28, 0x7fffffff, v18
	v_pk_fma_f32 v[20:21], v[22:23], v[20:21], s[4:5] op_sel_hi:[1,1,0]
	v_pk_fma_f32 v[28:29], v[28:29], s[14:15], 1.0 op_sel_hi:[1,0,0]
	v_pk_mul_f32 v[20:21], v[22:23], v[20:21]
	v_rcp_f32_e32 v28, v28
	v_rcp_f32_e32 v29, v29
	v_pk_mul_f32 v[20:21], v[26:27], v[20:21]
	v_cmp_gt_f32_e32 vcc, 0, v16
	v_pk_mul_f32 v[26:27], v[16:17], v[20:21]
	v_pk_fma_f32 v[20:21], v[16:17], v[20:21], v[16:17] neg_lo:[1,0,0] neg_hi:[1,0,0]
	v_pk_mul_f32 v[22:23], v[18:19], v[18:19]
	v_cndmask_b32_e32 v26, v20, v26, vcc
	v_cmp_gt_f32_e32 vcc, 0, v17
	v_pk_fma_f32 v[16:17], v[28:29], s[10:11], v[32:33] op_sel_hi:[1,0,0]
	v_pk_add_f32 v[4:5], v[4:5], v[8:9]
	v_cndmask_b32_e32 v27, v21, v27, vcc
	v_pk_mul_f32 v[20:21], v[22:23], s[6:7] op_sel_hi:[1,0]
	v_pk_fma_f32 v[16:17], v[28:29], v[16:17], s[12:13] op_sel_hi:[1,1,0]
	v_exp_f32_e32 v20, v20
	v_exp_f32_e32 v21, v21
	v_pk_fma_f32 v[16:17], v[28:29], v[16:17], s[0:1] op_sel_hi:[1,1,0]
	v_cmp_gt_f32_e32 vcc, 0, v18
	v_pk_fma_f32 v[16:17], v[28:29], v[16:17], s[4:5] op_sel_hi:[1,1,0]
	v_and_b32_e32 v9, 0x7fffffff, v5
	v_pk_mul_f32 v[16:17], v[28:29], v[16:17]
	v_and_b32_e32 v8, 0x7fffffff, v4
	v_pk_mul_f32 v[16:17], v[20:21], v[16:17]
	v_pk_fma_f32 v[8:9], v[8:9], s[14:15], 1.0 op_sel_hi:[1,0,0]
	v_pk_mul_f32 v[20:21], v[18:19], v[16:17]
	v_pk_fma_f32 v[16:17], v[18:19], v[16:17], v[18:19] neg_lo:[1,0,0] neg_hi:[1,0,0]
	v_rcp_f32_e32 v8, v8
	v_cndmask_b32_e32 v16, v16, v20, vcc
	v_cmp_gt_f32_e32 vcc, 0, v19
	v_or_b32_e32 v19, 48, v36
	v_rcp_f32_e32 v9, v9
	v_cndmask_b32_e32 v17, v17, v21, vcc
	v_cvt_pk_f16_f32 v17, v16, v17
	v_cvt_pk_f16_f32 v16, v26, v27
	ds_write_b64 v92, v[16:17] offset:8736
	v_mad_u64_u32 v[16:17], s[2:3], v19, s2, 0
	v_mov_b32_e32 v18, v17
	v_mad_u64_u32 v[18:19], s[2:3], v19, s1, v[18:19]
	v_mov_b32_e32 v17, v18
	v_pk_mul_f32 v[18:19], v[4:5], v[4:5]
	v_pk_add_f32 v[6:7], v[6:7], v[10:11]
	v_pk_fma_f32 v[10:11], v[8:9], s[10:11], v[32:33] op_sel_hi:[1,0,0]
	v_pk_mul_f32 v[18:19], v[18:19], s[6:7] op_sel_hi:[1,0]
	v_pk_fma_f32 v[10:11], v[8:9], v[10:11], s[12:13] op_sel_hi:[1,1,0]
	v_exp_f32_e32 v18, v18
	v_exp_f32_e32 v19, v19
	v_pk_fma_f32 v[10:11], v[8:9], v[10:11], s[0:1] op_sel_hi:[1,1,0]
	v_and_b32_e32 v21, 0x7fffffff, v7
	v_and_b32_e32 v20, 0x7fffffff, v6
	v_pk_fma_f32 v[10:11], v[8:9], v[10:11], s[4:5] op_sel_hi:[1,1,0]
	v_pk_fma_f32 v[20:21], v[20:21], s[14:15], 1.0 op_sel_hi:[1,0,0]
	v_pk_mul_f32 v[8:9], v[8:9], v[10:11]
	v_rcp_f32_e32 v20, v20
	v_rcp_f32_e32 v21, v21
	v_pk_mul_f32 v[8:9], v[18:19], v[8:9]
	v_cmp_gt_f32_e32 vcc, 0, v4
	v_pk_mul_f32 v[18:19], v[4:5], v[8:9]
	v_pk_fma_f32 v[8:9], v[4:5], v[8:9], v[4:5] neg_lo:[1,0,0] neg_hi:[1,0,0]
	v_pk_mul_f32 v[10:11], v[6:7], v[6:7]
	v_cndmask_b32_e32 v18, v8, v18, vcc
	v_cmp_gt_f32_e32 vcc, 0, v5
	v_pk_fma_f32 v[4:5], v[20:21], s[10:11], v[32:33] op_sel_hi:[1,0,0]
	v_pk_add_f32 v[0:1], v[0:1], v[12:13]
	v_cndmask_b32_e32 v19, v9, v19, vcc
	v_pk_mul_f32 v[8:9], v[10:11], s[6:7] op_sel_hi:[1,0]
	v_pk_fma_f32 v[4:5], v[20:21], v[4:5], s[12:13] op_sel_hi:[1,1,0]
	v_exp_f32_e32 v8, v8
	v_exp_f32_e32 v9, v9
	v_pk_fma_f32 v[4:5], v[20:21], v[4:5], s[0:1] op_sel_hi:[1,1,0]
	v_cmp_gt_f32_e32 vcc, 0, v6
	v_pk_fma_f32 v[4:5], v[20:21], v[4:5], s[4:5] op_sel_hi:[1,1,0]
	v_lshl_add_u64 v[16:17], v[16:17], 1, s[8:9]
	v_pk_mul_f32 v[4:5], v[20:21], v[4:5]
	v_pk_mul_f32 v[10:11], v[0:1], v[0:1]
	v_pk_mul_f32 v[4:5], v[8:9], v[4:5]
	v_pk_mul_f32 v[10:11], v[10:11], s[6:7] op_sel_hi:[1,0]
	v_pk_mul_f32 v[8:9], v[6:7], v[4:5]
	v_pk_fma_f32 v[4:5], v[6:7], v[4:5], v[6:7] neg_lo:[1,0,0] neg_hi:[1,0,0]
	v_and_b32_e32 v6, 0x7fffffff, v0
	v_cndmask_b32_e32 v4, v4, v8, vcc
	v_cmp_gt_f32_e32 vcc, 0, v7
	v_and_b32_e32 v7, 0x7fffffff, v1
	v_pk_fma_f32 v[6:7], v[6:7], s[14:15], 1.0 op_sel_hi:[1,0,0]
	v_cndmask_b32_e32 v5, v5, v9, vcc
	v_rcp_f32_e32 v6, v6
	v_rcp_f32_e32 v7, v7
	v_cvt_pk_f16_f32 v5, v4, v5
	v_cvt_pk_f16_f32 v4, v18, v19
	v_lshl_add_u64 v[8:9], v[16:17], 0, v[34:35]
	ds_write_b64 v92, v[4:5] offset:13056
	v_pk_fma_f32 v[4:5], v[6:7], s[10:11], v[32:33] op_sel_hi:[1,0,0]
	v_pk_add_f32 v[2:3], v[2:3], v[14:15]
	v_pk_fma_f32 v[4:5], v[6:7], v[4:5], s[12:13] op_sel_hi:[1,1,0]
	v_exp_f32_e32 v10, v10
	v_exp_f32_e32 v11, v11
	v_pk_fma_f32 v[4:5], v[6:7], v[4:5], s[0:1] op_sel_hi:[1,1,0]
	v_and_b32_e32 v13, 0x7fffffff, v3
	v_and_b32_e32 v12, 0x7fffffff, v2
	v_pk_fma_f32 v[4:5], v[6:7], v[4:5], s[4:5] op_sel_hi:[1,1,0]
	v_pk_fma_f32 v[12:13], v[12:13], s[14:15], 1.0 op_sel_hi:[1,0,0]
	v_pk_mul_f32 v[4:5], v[6:7], v[4:5]
	v_rcp_f32_e32 v12, v12
	v_rcp_f32_e32 v13, v13
	v_pk_mul_f32 v[4:5], v[10:11], v[4:5]
	v_cmp_gt_f32_e32 vcc, 0, v0
	v_pk_mul_f32 v[10:11], v[0:1], v[4:5]
	v_pk_fma_f32 v[4:5], v[0:1], v[4:5], v[0:1] neg_lo:[1,0,0] neg_hi:[1,0,0]
	v_pk_mul_f32 v[6:7], v[2:3], v[2:3]
	v_cndmask_b32_e32 v10, v4, v10, vcc
	v_cmp_gt_f32_e32 vcc, 0, v1
	v_pk_fma_f32 v[0:1], v[12:13], s[10:11], v[32:33] op_sel_hi:[1,0,0]
	s_nop 0
	v_cndmask_b32_e32 v11, v5, v11, vcc
	v_pk_mul_f32 v[4:5], v[6:7], s[6:7] op_sel_hi:[1,0]
	v_pk_fma_f32 v[0:1], v[12:13], v[0:1], s[12:13] op_sel_hi:[1,1,0]
	v_exp_f32_e32 v4, v4
	v_exp_f32_e32 v5, v5
	v_pk_fma_f32 v[0:1], v[12:13], v[0:1], s[0:1] op_sel_hi:[1,1,0]
	v_cmp_gt_f32_e32 vcc, 0, v2
	v_pk_fma_f32 v[0:1], v[12:13], v[0:1], s[4:5] op_sel_hi:[1,1,0]
	s_nop 0
	v_pk_mul_f32 v[0:1], v[12:13], v[0:1]
	s_nop 0
	v_pk_mul_f32 v[0:1], v[4:5], v[0:1]
	s_nop 0
	v_pk_mul_f32 v[4:5], v[2:3], v[0:1]
	v_pk_fma_f32 v[0:1], v[2:3], v[0:1], v[2:3] neg_lo:[1,0,0] neg_hi:[1,0,0]
	s_nop 0
	v_cndmask_b32_e32 v0, v0, v4, vcc
	v_cmp_gt_f32_e32 vcc, 0, v3
	s_nop 1
	v_cndmask_b32_e32 v1, v1, v5, vcc
	v_cvt_pk_f16_f32 v1, v0, v1
	v_cvt_pk_f16_f32 v0, v10, v11
	ds_write_b64 v92, v[0:1] offset:13088
	s_waitcnt lgkmcnt(0)
	s_barrier
	ds_read_b128 v[72:75], v94
	ds_read_b128 v[76:79], v94 offset:8704
	ds_read_b128 v[80:83], v94 offset:17408
	ds_read_b128 v[84:87], v94 offset:26112
	s_waitcnt lgkmcnt(3)
	global_store_dwordx4 v95, v[72:75], s[24:25] sc1
	s_waitcnt lgkmcnt(2)
	global_store_dwordx4 v95, v[76:79], s[26:27] sc1
	s_waitcnt lgkmcnt(1)
	global_store_dwordx4 v95, v[80:83], s[28:29] sc1
	s_waitcnt lgkmcnt(0)
	global_store_dwordx4 v95, v[84:87], s[30:31] sc1
	s_endpgm
	s_endpgm
	s_endpgm
	s_endpgm
	s_endpgm
	s_endpgm
	s_endpgm
	s_endpgm
	s_endpgm
	s_endpgm
	s_endpgm
	s_endpgm
	s_endpgm
	s_endpgm
	s_endpgm
	s_endpgm
	s_endpgm
	s_endpgm
	s_endpgm
	s_endpgm
	s_endpgm
	s_endpgm
	s_endpgm
	s_endpgm

	.amdhsa_kernel _Z5gemm8ILi128ELi2ELi2ELi2ELi1ELi16EEvPKDF16_S1_iiiPDF16_PfPKf
		.amdhsa_group_segment_fixed_size 0
		.amdhsa_private_segment_fixed_size 0
		.amdhsa_kernarg_size 312
		.amdhsa_user_sgpr_count 2
		.amdhsa_user_sgpr_dispatch_ptr 0
		.amdhsa_user_sgpr_queue_ptr 0
		.amdhsa_user_sgpr_kernarg_segment_ptr 1
		.amdhsa_user_sgpr_dispatch_id 0
		.amdhsa_user_sgpr_kernarg_preload_length 0
		.amdhsa_user_sgpr_kernarg_preload_offset 0
		.amdhsa_user_sgpr_private_segment_size 0
		.amdhsa_uses_dynamic_stack 0
		.amdhsa_enable_private_segment 0
		.amdhsa_system_sgpr_workgroup_id_x 1
		.amdhsa_system_sgpr_workgroup_id_y 0
		.amdhsa_system_sgpr_workgroup_id_z 0
		.amdhsa_system_sgpr_workgroup_info 0
		.amdhsa_system_vgpr_workitem_id 0
		.amdhsa_next_free_vgpr 96
		.amdhsa_next_free_sgpr 32
		.amdhsa_accum_offset 96
		.amdhsa_reserve_vcc 1
		.amdhsa_float_round_mode_32 0
		.amdhsa_float_round_mode_16_64 0
		.amdhsa_float_denorm_mode_32 3
		.amdhsa_float_denorm_mode_16_64 3
		.amdhsa_dx10_clamp 1
		.amdhsa_ieee_mode 1
		.amdhsa_fp16_overflow 0
		.amdhsa_tg_split 0
		.amdhsa_exception_fp_ieee_invalid_op 0
		.amdhsa_exception_fp_denorm_src 0
		.amdhsa_exception_fp_ieee_div_zero 0
		.amdhsa_exception_fp_ieee_overflow 0
		.amdhsa_exception_fp_ieee_underflow 0
		.amdhsa_exception_fp_ieee_inexact 0
		.amdhsa_exception_int_div_zero 0
	.end_amdhsa_kernel

amdhsa.kernels:
  - .agpr_count:     0
    .args:
      - .offset:         0
        .size:           400
        .value_kind:     by_value
    .group_segment_fixed_size: 33280
    .kernarg_segment_align: 8
    .kernarg_segment_size: 400
    .language:       OpenCL C
    .language_version:
      - 2
      - 0
    .max_flat_workgroup_size: 256
    .name:           _Z10wt_convert7CvtJobs
    .private_segment_fixed_size: 0
    .sgpr_count:     54
    .sgpr_spill_count: 0
    .symbol:         _Z10wt_convert7CvtJobs.kd
    .uniform_work_group_size: 1
    .uses_dynamic_stack: false
    .vgpr_count:     45
    .vgpr_spill_count: 0
    .wavefront_size: 64
  - .agpr_count:     0
    .args:
      - .actual_access:  read_only
        .address_space:  global
        .offset:         0
        .size:           8
        .value_kind:     global_buffer
      - .actual_access:  read_only
        .address_space:  global
        .offset:         8
        .size:           8
        .value_kind:     global_buffer
      - .actual_access:  read_only
        .address_space:  global
        .offset:         16
        .size:           8
        .value_kind:     global_buffer
      - .actual_access:  write_only
        .address_space:  global
        .offset:         24
        .size:           8
        .value_kind:     global_buffer
      - .actual_access:  read_only
        .address_space:  global
        .offset:         32
        .size:           8
        .value_kind:     global_buffer
      - .actual_access:  read_only
        .address_space:  global
        .offset:         40
        .size:           8
        .value_kind:     global_buffer
      - .actual_access:  write_only
        .address_space:  global
        .offset:         48
        .size:           8
        .value_kind:     global_buffer
      - .offset:         56
        .size:           400
        .value_kind:     by_value
    .group_segment_fixed_size: 33280
    .kernarg_segment_align: 8
    .kernarg_segment_size: 456
    .language:       OpenCL C
    .language_version:
      - 2
      - 0
    .max_flat_workgroup_size: 256
    .name:           _Z13embed_ln_convPKiPKfS2_PfS2_S2_PDF16_7CvtJobs
    .private_segment_fixed_size: 0
    .sgpr_count:     36
    .sgpr_spill_count: 0
    .symbol:         _Z13embed_ln_convPKiPKfS2_PfS2_S2_PDF16_7CvtJobs.kd
    .uniform_work_group_size: 1
    .uses_dynamic_stack: false
    .vgpr_count:     79
    .vgpr_spill_count: 0
    .wavefront_size: 64
  - .agpr_count:     0
    .args:
      - .address_space:  global
        .offset:         0
        .size:           8
        .value_kind:     global_buffer
      - .address_space:  global
        .offset:         8
        .size:           8
        .value_kind:     global_buffer
      - .actual_access:  write_only
        .address_space:  global
        .offset:         16
        .size:           8
        .value_kind:     global_buffer
      - .actual_access:  read_only
        .address_space:  global
        .offset:         24
        .size:           8
        .value_kind:     global_buffer
      - .offset:         32
        .size:           4
        .value_kind:     by_value
      - .offset:         36
        .size:           4
        .value_kind:     by_value
      - .offset:         40
        .size:           4
        .value_kind:     by_value
    .group_segment_fixed_size: 0
    .kernarg_segment_align: 8
    .kernarg_segment_size: 44
    .language:       OpenCL C
    .language_version:
      - 2
      - 0
    .max_flat_workgroup_size: 512
    .name:           _Z17gemm_256sq_8phasePKDF16_S0_PfPKfiii
    .private_segment_fixed_size: 0
    .sgpr_count:     47
    .sgpr_spill_count: 0
    .symbol:         _Z17gemm_256sq_8phasePKDF16_S0_PfPKfiii.kd
    .uniform_work_group_size: 1
    .uses_dynamic_stack: false
    .vgpr_count:     244
    .vgpr_spill_count: 0
    .wavefront_size: 64
  - .agpr_count:     0
    .args:
      - .actual_access:  read_only
        .address_space:  global
        .offset:         0
        .size:           8
        .value_kind:     global_buffer
      - .actual_access:  read_only
        .address_space:  global
        .offset:         8
        .size:           8
        .value_kind:     global_buffer
      - .actual_access:  read_only
        .address_space:  global
        .offset:         16
        .size:           8
        .value_kind:     global_buffer
      - .actual_access:  write_only
        .address_space:  global
        .offset:         24
        .size:           8
        .value_kind:     global_buffer
      - .offset:         32
        .size:           400
        .value_kind:     by_value
    .group_segment_fixed_size: 33280
    .kernarg_segment_align: 8
    .kernarg_segment_size: 432
    .language:       OpenCL C
    .language_version:
      - 2
      - 0
    .max_flat_workgroup_size: 256
    .name:           _Z11attn_kernelPKDF16_S0_S0_PDF16_7CvtJobs
    .private_segment_fixed_size: 0
    .sgpr_count:     36
    .sgpr_spill_count: 0
    .symbol:         _Z11attn_kernelPKDF16_S0_S0_PDF16_7CvtJobs.kd
    .uniform_work_group_size: 1
    .uses_dynamic_stack: false
    .vgpr_count:     116
    .vgpr_spill_count: 0
    .wavefront_size: 64
  - .agpr_count:     0
    .args:
      - .address_space:  global
        .offset:         0
        .size:           8
        .value_kind:     global_buffer
      - .address_space:  global
        .offset:         8
        .size:           8
        .value_kind:     global_buffer
      - .offset:         16
        .size:           4
        .value_kind:     by_value
      - .offset:         20
        .size:           4
        .value_kind:     by_value
      - .offset:         24
        .size:           4
        .value_kind:     by_value
      - .actual_access:  write_only
        .address_space:  global
        .offset:         32
        .size:           8
        .value_kind:     global_buffer
      - .actual_access:  read_only
        .address_space:  global
        .offset:         40
        .size:           8
        .value_kind:     global_buffer
      - .actual_access:  read_only
        .address_space:  global
        .offset:         48
        .size:           8
        .value_kind:     global_buffer
      - .offset:         56
        .size:           4
        .value_kind:     hidden_block_count_x
      - .offset:         60
        .size:           4
        .value_kind:     hidden_block_count_y
      - .offset:         64
        .size:           4
        .value_kind:     hidden_block_count_z
      - .offset:         68
        .size:           2
        .value_kind:     hidden_group_size_x
      - .offset:         70
        .size:           2
        .value_kind:     hidden_group_size_y
      - .offset:         72
        .size:           2
        .value_kind:     hidden_group_size_z
      - .offset:         74
        .size:           2
        .value_kind:     hidden_remainder_x
      - .offset:         76
        .size:           2
        .value_kind:     hidden_remainder_y
      - .offset:         78
        .size:           2
        .value_kind:     hidden_remainder_z
      - .offset:         96
        .size:           8
        .value_kind:     hidden_global_offset_x
      - .offset:         104
        .size:           8
        .value_kind:     hidden_global_offset_y
      - .offset:         112
        .size:           8
        .value_kind:     hidden_global_offset_z
      - .offset:         120
        .size:           2
        .value_kind:     hidden_grid_dims
      - .offset:         176
        .size:           4
        .value_kind:     hidden_dynamic_lds_size
    .group_segment_fixed_size: 0
    .kernarg_segment_align: 8
    .kernarg_segment_size: 312
    .language:       OpenCL C
    .language_version:
      - 2
      - 0
    .max_flat_workgroup_size: 512
    .name:           _Z5gemm8ILi192ELi2ELi3ELi0ELi1ELi16EEvPKDF16_S1_iiiPDF16_PfPKf
    .private_segment_fixed_size: 0
    .sgpr_count:     34
    .sgpr_spill_count: 0
    .symbol:         _Z5gemm8ILi192ELi2ELi3ELi0ELi1ELi16EEvPKDF16_S1_iiiPDF16_PfPKf.kd
    .uniform_work_group_size: 1
    .uses_dynamic_stack: false
    .vgpr_count:     125
    .vgpr_spill_count: 0
    .wavefront_size: 64
  - .agpr_count:     0
    .args:
      - .address_space:  global
        .offset:         0
        .size:           8
        .value_kind:     global_buffer
      - .address_space:  global
        .offset:         8
        .size:           8
        .value_kind:     global_buffer
      - .offset:         16
        .size:           4
        .value_kind:     by_value
      - .offset:         20
        .size:           4
        .value_kind:     by_value
      - .offset:         24
        .size:           4
        .value_kind:     by_value
      - .actual_access:  write_only
        .address_space:  global
        .offset:         32
        .size:           8
        .value_kind:     global_buffer
      - .actual_access:  read_only
        .address_space:  global
        .offset:         40
        .size:           8
        .value_kind:     global_buffer
      - .actual_access:  read_only
        .address_space:  global
        .offset:         48
        .size:           8
        .value_kind:     global_buffer
      - .offset:         56
        .size:           4
        .value_kind:     hidden_block_count_x
      - .offset:         60
        .size:           4
        .value_kind:     hidden_block_count_y
      - .offset:         64
        .size:           4
        .value_kind:     hidden_block_count_z
      - .offset:         68
        .size:           2
        .value_kind:     hidden_group_size_x
      - .offset:         70
        .size:           2
        .value_kind:     hidden_group_size_y
      - .offset:         72
        .size:           2
        .value_kind:     hidden_group_size_z
      - .offset:         74
        .size:           2
        .value_kind:     hidden_remainder_x
      - .offset:         76
        .size:           2
        .value_kind:     hidden_remainder_y
      - .offset:         78
        .size:           2
        .value_kind:     hidden_remainder_z
      - .offset:         96
        .size:           8
        .value_kind:     hidden_global_offset_x
      - .offset:         104
        .size:           8
        .value_kind:     hidden_global_offset_y
      - .offset:         112
        .size:           8
        .value_kind:     hidden_global_offset_z
      - .offset:         120
        .size:           2
        .value_kind:     hidden_grid_dims
      - .offset:         176
        .size:           4
        .value_kind:     hidden_dynamic_lds_size
    .group_segment_fixed_size: 0
    .kernarg_segment_align: 8
    .kernarg_segment_size: 312
    .language:       OpenCL C
    .language_version:
      - 2
      - 0
    .max_flat_workgroup_size: 512
    .name:           _Z5gemm8ILi128ELi2ELi2ELi2ELi1ELi16EEvPKDF16_S1_iiiPDF16_PfPKf
    .private_segment_fixed_size: 0
    .sgpr_count:     38
    .sgpr_spill_count: 0
    .symbol:         _Z5gemm8ILi128ELi2ELi2ELi2ELi1ELi16EEvPKDF16_S1_iiiPDF16_PfPKf.kd
    .uniform_work_group_size: 1
    .uses_dynamic_stack: false
    .vgpr_count:     96
    .vgpr_spill_count: 0
    .wavefront_size: 64
  - .agpr_count:     0
    .args:
      - .address_space:  global
        .offset:         0
        .size:           8
        .value_kind:     global_buffer
      - .address_space:  global
        .offset:         8
        .size:           8
        .value_kind:     global_buffer
      - .offset:         16
        .size:           4
        .value_kind:     by_value
      - .offset:         20
        .size:           4
        .value_kind:     by_value
      - .offset:         24
        .size:           4
        .value_kind:     by_value
      - .actual_access:  read_only
        .address_space:  global
        .offset:         32
        .size:           8
        .value_kind:     global_buffer
      - .address_space:  global
        .offset:         40
        .size:           8
        .value_kind:     global_buffer
      - .actual_access:  read_only
        .address_space:  global
        .offset:         48
        .size:           8
        .value_kind:     global_buffer
      - .offset:         56
        .size:           4
        .value_kind:     hidden_block_count_x
      - .offset:         60
        .size:           4
        .value_kind:     hidden_block_count_y
      - .offset:         64
        .size:           4
        .value_kind:     hidden_block_count_z
      - .offset:         68
        .size:           2
        .value_kind:     hidden_group_size_x
      - .offset:         70
        .size:           2
        .value_kind:     hidden_group_size_y
      - .offset:         72
        .size:           2
        .value_kind:     hidden_group_size_z
      - .offset:         74
        .size:           2
        .value_kind:     hidden_remainder_x
      - .offset:         76
        .size:           2
        .value_kind:     hidden_remainder_y
      - .offset:         78
        .size:           2
        .value_kind:     hidden_remainder_z
      - .offset:         96
        .size:           8
        .value_kind:     hidden_global_offset_x
      - .offset:         104
        .size:           8
        .value_kind:     hidden_global_offset_y
      - .offset:         112
        .size:           8
        .value_kind:     hidden_global_offset_z
      - .offset:         120
        .size:           2
        .value_kind:     hidden_grid_dims
      - .offset:         176
        .size:           4
        .value_kind:     hidden_dynamic_lds_size
    .group_segment_fixed_size: 0
    .kernarg_segment_align: 8
    .kernarg_segment_size: 312
    .language:       OpenCL C
    .language_version:
      - 2
      - 0
    .max_flat_workgroup_size: 512
    .name:           _Z5gemm8ILi64ELi4ELi6ELi1ELi1ELi16EEvPKDF16_S1_iiiPDF16_PfPKf
    .private_segment_fixed_size: 0
    .sgpr_count:     34
    .sgpr_spill_count: 0
    .symbol:         _Z5gemm8ILi64ELi4ELi6ELi1ELi1ELi16EEvPKDF16_S1_iiiPDF16_PfPKf.kd
    .uniform_work_group_size: 1
    .uses_dynamic_stack: false
    .vgpr_count:     104
    .vgpr_spill_count: 0
    .wavefront_size: 64
  - .agpr_count:     0
    .args:
      - .address_space:  global
        .offset:         0
        .size:           8
        .value_kind:     global_buffer
      - .address_space:  global
        .offset:         8
        .size:           8
        .value_kind:     global_buffer
      - .offset:         16
        .size:           4
        .value_kind:     by_value
      - .offset:         20
        .size:           4
        .value_kind:     by_value
      - .offset:         24
        .size:           4
        .value_kind:     by_value
      - .actual_access:  write_only
        .address_space:  global
        .offset:         32
        .size:           8
        .value_kind:     global_buffer
      - .actual_access:  read_only
        .address_space:  global
        .offset:         40
        .size:           8
        .value_kind:     global_buffer
      - .actual_access:  read_only
        .address_space:  global
        .offset:         48
        .size:           8
        .value_kind:     global_buffer
    .group_segment_fixed_size: 0
    .kernarg_segment_align: 8
    .kernarg_segment_size: 56
    .language:       OpenCL C
    .language_version:
      - 2
      - 0
    .max_flat_workgroup_size: 512
    .name:           _Z5gemm8ILi128ELi2ELi4ELi4ELi2ELi32EEvPKDF16_S1_iiiPDF16_PfPKf
    .private_segment_fixed_size: 0
    .sgpr_count:     38
    .sgpr_spill_count: 0
    .symbol:         _Z5gemm8ILi128ELi2ELi4ELi4ELi2ELi32EEvPKDF16_S1_iiiPDF16_PfPKf.kd
    .uniform_work_group_size: 1
    .uses_dynamic_stack: false
    .vgpr_count:     107
    .vgpr_spill_count: 0
    .wavefront_size: 64
  - .agpr_count:     0
    .args:
      - .actual_access:  read_only
        .address_space:  global
        .offset:         0
        .size:           8
        .value_kind:     global_buffer
      - .actual_access:  read_only
        .address_space:  global
        .offset:         8
        .size:           8
        .value_kind:     global_buffer
      - .actual_access:  read_only
        .address_space:  global
        .offset:         16
        .size:           8
        .value_kind:     global_buffer
      - .address_space:  global
        .offset:         24
        .size:           8
        .value_kind:     global_buffer
      - .actual_access:  read_only
        .address_space:  global
        .offset:         32
        .size:           8
        .value_kind:     global_buffer
      - .actual_access:  read_only
        .address_space:  global
        .offset:         40
        .size:           8
        .value_kind:     global_buffer
      - .actual_access:  write_only
        .address_space:  global
        .offset:         48
        .size:           8
        .value_kind:     global_buffer
    .group_segment_fixed_size: 0
    .kernarg_segment_align: 8
    .kernarg_segment_size: 56
    .language:       OpenCL C
    .language_version:
      - 2
      - 0
    .max_flat_workgroup_size: 256
    .name:           _Z9ln_kernelILi2EEvPKiPKfS3_PfS3_S3_PDF16_
    .private_segment_fixed_size: 0
    .sgpr_count:     18
    .sgpr_spill_count: 0
    .symbol:         _Z9ln_kernelILi2EEvPKiPKfS3_PfS3_S3_PDF16_.kd
    .uniform_work_group_size: 1
    .uses_dynamic_stack: false
    .vgpr_count:     88
    .vgpr_spill_count: 0
    .wavefront_size: 64
  - .agpr_count:     0
    .args:
      - .actual_access:  read_only
        .address_space:  global
        .offset:         0
        .size:           8
        .value_kind:     global_buffer
      - .actual_access:  read_only
        .address_space:  global
        .offset:         8
        .size:           8
        .value_kind:     global_buffer
      - .actual_access:  read_only
        .address_space:  global
        .offset:         16
        .size:           8
        .value_kind:     global_buffer
      - .actual_access:  read_only
        .address_space:  global
        .offset:         24
        .size:           8
        .value_kind:     global_buffer
      - .actual_access:  read_only
        .address_space:  global
        .offset:         32
        .size:           8
        .value_kind:     global_buffer
      - .actual_access:  read_only
        .address_space:  global
        .offset:         40
        .size:           8
        .value_kind:     global_buffer
      - .actual_access:  write_only
        .address_space:  global
        .offset:         48
        .size:           8
        .value_kind:     global_buffer
    .group_segment_fixed_size: 0
    .kernarg_segment_align: 8
    .kernarg_segment_size: 56
    .language:       OpenCL C
    .language_version:
      - 2
      - 0
    .max_flat_workgroup_size: 256
    .name:           _Z9ln_kernelILi0EEvPKiPKfS3_PfS3_S3_PDF16_
    .private_segment_fixed_size: 0
    .sgpr_count:     18
    .sgpr_spill_count: 0
    .symbol:         _Z9ln_kernelILi0EEvPKiPKfS3_PfS3_S3_PDF16_.kd
    .uniform_work_group_size: 1
    .uses_dynamic_stack: false
    .vgpr_count:     60
    .vgpr_spill_count: 0
    .wavefront_size: 64
  - .agpr_count:     0
    .args:
      - .actual_access:  read_only
        .address_space:  global
        .offset:         0
        .size:           8
        .value_kind:     global_buffer
      - .actual_access:  read_only
        .address_space:  global
        .offset:         8
        .size:           8
        .value_kind:     global_buffer
      - .actual_access:  read_only
        .address_space:  global
        .offset:         16
        .size:           8
        .value_kind:     global_buffer
      - .actual_access:  read_only
        .address_space:  global
        .offset:         24
        .size:           8
        .value_kind:     global_buffer
      - .actual_access:  read_only
        .address_space:  global
        .offset:         32
        .size:           8
        .value_kind:     global_buffer
      - .actual_access:  read_only
        .address_space:  global
        .offset:         40
        .size:           8
        .value_kind:     global_buffer
      - .actual_access:  write_only
        .address_space:  global
        .offset:         48
        .size:           8
        .value_kind:     global_buffer
    .group_segment_fixed_size: 0
    .kernarg_segment_align: 8
    .kernarg_segment_size: 56
    .language:       OpenCL C
    .language_version:
      - 2
      - 0
    .max_flat_workgroup_size: 256
    .name:           _Z9ln_kernelILi4EEvPKiPKfS3_PfS3_S3_PDF16_
    .private_segment_fixed_size: 0
    .sgpr_count:     18
    .sgpr_spill_count: 0
    .symbol:         _Z9ln_kernelILi4EEvPKiPKfS3_PfS3_S3_PDF16_.kd
    .uniform_work_group_size: 1
    .uses_dynamic_stack: false
    .vgpr_count:     64
    .vgpr_spill_count: 0
    .wavefront_size: 64
